# P0 conversion phase: bf16 weight stores made non-temporal (nt)
# speedup vs baseline: 1.0122x; 1.0122x over previous
; __device__ __forceinline__ unsigned pk2(float lo, float hi) { unsigned r; asm("v_cvt_pk_bf16_f32 %0, %1, %2" : "=v"(r) : "v"(lo), "v"(hi)); return r; }
; __device__ __forceinline__ void phase_convert(const Ctx& c) {
;     ...
;           for (int q = 0; q < 8; ++q) { const long i = i0 + (long)q * c.gthreads; v[q] = (f32x4){0.f, 0.f, 0.f, 0.f}; if (i < (long)T * D / 4) v[q] = __builtin_nontemporal_load((const f32x4*)(x + i * 4)); }
; #pragma unroll
;           for (int q = 0; q < 8; ++q) { const long i = i0 + (long)q * c.gthreads; if (i < (long)T * D / 4) { u32x2 w; w[0] = pk2(v[q][0], v[q][1]); w[1] = pk2(v[q][2], v[q][3]); *(u32x2*)(xb + i * 4) = w; } } } }
.LBB0_27:
	s_or_b64 exec, exec, s[44:45]
	s_waitcnt vmcnt(0)
	v_cvt_pk_bf16_f32 v8, v8, v9
	v_cvt_pk_bf16_f32 v9, v10, v11
	v_lshl_add_u64 v[10:11], s[42:43], 0, v[32:33]
	global_store_dwordx2 v[10:11], v[8:9], off nt
	s_and_saveexec_b64 s[44:45], vcc
	s_cbranch_execz .LBB0_34
	v_cvt_pk_bf16_f32 v4, v4, v5
	v_cvt_pk_bf16_f32 v5, v6, v7
	v_lshl_add_u64 v[6:7], s[42:43], 0, v[62:63]
	global_store_dwordx2 v[6:7], v[4:5], off nt
	s_or_b64 exec, exec, s[44:45]
	s_and_saveexec_b64 s[44:45], s[2:3]
	s_cbranch_execnz .LBB0_35

; __device__ __forceinline__ unsigned pk2(float lo, float hi) { unsigned r; asm("v_cvt_pk_bf16_f32 %0, %1, %2" : "=v"(r) : "v"(lo), "v"(hi)); return r; }
; __device__ __forceinline__ void phase_convert(const Ctx& c) {
;     ...
;           for (int q = 0; q < 8; ++q) { const long i = i0 + (long)q * c.gthreads; v[q] = (f32x4){0.f, 0.f, 0.f, 0.f}; if (i < (long)T * D / 4) v[q] = __builtin_nontemporal_load((const f32x4*)(x + i * 4)); }
; #pragma unroll
;           for (int q = 0; q < 8; ++q) { const long i = i0 + (long)q * c.gthreads; if (i < (long)T * D / 4) { u32x2 w; w[0] = pk2(v[q][0], v[q][1]); w[1] = pk2(v[q][2], v[q][3]); *(u32x2*)(xb + i * 4) = w; } } } }
.LBB0_30:
	v_cvt_pk_bf16_f32 v0, v0, v1
	v_cvt_pk_bf16_f32 v1, v2, v3
	v_lshl_add_u64 v[2:3], s[42:43], 0, v[44:45]
	global_store_dwordx2 v[2:3], v[0:1], off nt
	s_or_b64 exec, exec, s[2:3]
	s_and_saveexec_b64 s[2:3], s[6:7]
	s_cbranch_execnz .LBB0_37

; __device__ __forceinline__ unsigned pk2(float lo, float hi) { unsigned r; asm("v_cvt_pk_bf16_f32 %0, %1, %2" : "=v"(r) : "v"(lo), "v"(hi)); return r; }
; __device__ __forceinline__ void phase_convert(const Ctx& c) {
;     ...
;           for (int q = 0; q < 8; ++q) { const long i = i0 + (long)q * c.gthreads; v[q] = (f32x4){0.f, 0.f, 0.f, 0.f}; if (i < (long)T * D / 4) v[q] = __builtin_nontemporal_load((const f32x4*)(x + i * 4)); }
; #pragma unroll
;           for (int q = 0; q < 8; ++q) { const long i = i0 + (long)q * c.gthreads; if (i < (long)T * D / 4) { u32x2 w; w[0] = pk2(v[q][0], v[q][1]); w[1] = pk2(v[q][2], v[q][3]); *(u32x2*)(xb + i * 4) = w; } } } }
.LBB0_32:
	v_lshl_add_u64 v[2:3], s[42:43], 0, v[52:53]
	v_cvt_pk_bf16_f32 v0, v16, v17
	v_cvt_pk_bf16_f32 v1, v18, v19
	global_store_dwordx2 v[2:3], v[0:1], off nt
	s_or_b64 exec, exec, s[2:3]
	s_and_saveexec_b64 s[2:3], s[10:11]
	s_cbranch_execnz .LBB0_39

; __device__ __forceinline__ unsigned pk2(float lo, float hi) { unsigned r; asm("v_cvt_pk_bf16_f32 %0, %1, %2" : "=v"(r) : "v"(lo), "v"(hi)); return r; }
; __device__ __forceinline__ void phase_convert(const Ctx& c) {
;     ...
;           for (int q = 0; q < 8; ++q) { const long i = i0 + (long)q * c.gthreads; v[q] = (f32x4){0.f, 0.f, 0.f, 0.f}; if (i < (long)T * D / 4) v[q] = __builtin_nontemporal_load((const f32x4*)(x + i * 4)); }
; #pragma unroll
;           for (int q = 0; q < 8; ++q) { const long i = i0 + (long)q * c.gthreads; if (i < (long)T * D / 4) { u32x2 w; w[0] = pk2(v[q][0], v[q][1]); w[1] = pk2(v[q][2], v[q][3]); *(u32x2*)(xb + i * 4) = w; } } } }
.LBB0_35:
	v_lshl_add_u64 v[6:7], s[42:43], 0, v[40:41]
	v_cvt_pk_bf16_f32 v4, v12, v13
	v_cvt_pk_bf16_f32 v5, v14, v15
	global_store_dwordx2 v[6:7], v[4:5], off nt
	s_or_b64 exec, exec, s[44:45]
	s_and_saveexec_b64 s[2:3], s[4:5]
	s_cbranch_execnz .LBB0_30

; __device__ __forceinline__ unsigned pk2(float lo, float hi) { unsigned r; asm("v_cvt_pk_bf16_f32 %0, %1, %2" : "=v"(r) : "v"(lo), "v"(hi)); return r; }
; __device__ __forceinline__ void phase_convert(const Ctx& c) {
;     ...
;           for (int q = 0; q < 8; ++q) { const long i = i0 + (long)q * c.gthreads; v[q] = (f32x4){0.f, 0.f, 0.f, 0.f}; if (i < (long)T * D / 4) v[q] = __builtin_nontemporal_load((const f32x4*)(x + i * 4)); }
; #pragma unroll
;           for (int q = 0; q < 8; ++q) { const long i = i0 + (long)q * c.gthreads; if (i < (long)T * D / 4) { u32x2 w; w[0] = pk2(v[q][0], v[q][1]); w[1] = pk2(v[q][2], v[q][3]); *(u32x2*)(xb + i * 4) = w; } } } }
.LBB0_37:
	v_lshl_add_u64 v[2:3], s[42:43], 0, v[48:49]
	v_cvt_pk_bf16_f32 v0, v20, v21
	v_cvt_pk_bf16_f32 v1, v22, v23
	global_store_dwordx2 v[2:3], v[0:1], off nt
	s_or_b64 exec, exec, s[2:3]
	s_and_saveexec_b64 s[2:3], s[8:9]
	s_cbranch_execnz .LBB0_32

; __device__ __forceinline__ unsigned pk2(float lo, float hi) { unsigned r; asm("v_cvt_pk_bf16_f32 %0, %1, %2" : "=v"(r) : "v"(lo), "v"(hi)); return r; }
; __device__ __forceinline__ void phase_convert(const Ctx& c) {
;     ...
;           for (int q = 0; q < 8; ++q) { const long i = i0 + (long)q * c.gthreads; v[q] = (f32x4){0.f, 0.f, 0.f, 0.f}; if (i < (long)T * D / 4) v[q] = __builtin_nontemporal_load((const f32x4*)(x + i * 4)); }
; #pragma unroll
;           for (int q = 0; q < 8; ++q) { const long i = i0 + (long)q * c.gthreads; if (i < (long)T * D / 4) { u32x2 w; w[0] = pk2(v[q][0], v[q][1]); w[1] = pk2(v[q][2], v[q][3]); *(u32x2*)(xb + i * 4) = w; } } } }
.LBB0_39:
	v_lshl_add_u64 v[2:3], s[42:43], 0, v[56:57]
	v_cvt_pk_bf16_f32 v0, v28, v29
	v_cvt_pk_bf16_f32 v1, v30, v31
	global_store_dwordx2 v[2:3], v[0:1], off nt
	s_or_b64 exec, exec, s[2:3]
	s_and_saveexec_b64 s[2:3], s[12:13]
	s_cbranch_execz .LBB0_12
.LBB0_40:
	v_lshl_add_u64 v[2:3], s[42:43], 0, v[60:61]
	v_cvt_pk_bf16_f32 v0, v24, v25
	v_cvt_pk_bf16_f32 v1, v26, v27
	global_store_dwordx2 v[2:3], v[0:1], off nt
	s_branch .LBB0_12

; __device__ __forceinline__ void phase_convert(const Ctx& c) {
;     ...
;     { bf16_t* wrt = (bf16_t*)(ws + WS_WRT); for (long i = c.gtid; i < (long)4 * 128 * D / 8; i += c.gthreads) { const long l = i / (128 * D / 8), r = i % (128 * D / 8); *(u32x4*)(wrt + (size_t)l * 256 * D + (size_t)128 * D + r * 8) = (u32x4){0u, 0u, 0u, 0u}; }
.LBB0_43:
	v_ashrrev_i32_e32 v2, 31, v5
	v_lshrrev_b32_e32 v2, 18, v2
	v_lshl_add_u64 v[10:11], v[4:5], 0, v[2:3]
	v_lshl_add_u64 v[4:5], v[4:5], 0, s[18:19]
	v_lshlrev_b64 v[10:11], 4, v[10:11]
	v_cmp_lt_i64_e32 vcc, s[8:9], v[4:5]
	v_and_b32_e32 v10, 0xfffc0000, v10
	s_or_b64 s[6:7], vcc, s[6:7]
	v_lshl_add_u64 v[10:11], v[0:1], 0, v[10:11]
	v_lshl_add_u64 v[0:1], v[0:1], 0, s[4:5]
	global_store_dwordx4 v[10:11], v[6:9], off nt
	s_andn2_b64 exec, exec, s[6:7]
	s_cbranch_execnz .LBB0_43

; __device__ __forceinline__ unsigned pk2(float lo, float hi) { unsigned r; asm("v_cvt_pk_bf16_f32 %0, %1, %2" : "=v"(r) : "v"(lo), "v"(hi)); return r; }
; template <int TN, class DstFn>
; __device__ __forceinline__ void convert_T(const Ctx& c, const float* src, int nmat, int K, int N, DstFn dstfn) {
;     ...
;         { const int ch = c.tid & 7, nb = c.tid >> 3;
; #pragma unroll
;           for (int j = 0; j < TN / 64; ++j) { const int n = nb + 64 * j;
;               bf16_t* d = dstfn(m, nt * TN + n) + kt * 64 + ch * 8; u32x4 w;
; #pragma unroll
;               for (int e = 0; e < 4; ++e) w[e] = pk2(tile[(ch * 8 + 2 * e) * LDT + n], tile[(ch * 8 + 2 * e + 1) * LDT + n]);
;               *(u32x4*)d = w; } }
;         __syncthreads();
.LBB0_73:
	s_or_b64 exec, exec, s[10:11]
	ds_read_b32 v83, v62 offset:768
	ds_read_b32 v84, v62 offset:1796
	ds_read_b32 v85, v62 offset:2824
	ds_read_b32 v86, v62 offset:3852
	ds_read_b32 v87, v62 offset:4880
	ds_read_b32 v88, v62 offset:5908
	ds_read_b32 v89, v62 offset:6936
	ds_read_b32 v90, v62 offset:7964
	v_ashrrev_i32_e32 v61, 31, v60
	v_lshlrev_b64 v[60:61], 11, v[60:61]
	v_lshl_add_u64 v[58:59], v[58:59], 0, v[60:61]
	s_andn2_b64 vcc, exec, s[2:3]
	s_mov_b64 s[10:11], s[8:9]
	s_waitcnt lgkmcnt(6)
	v_cvt_pk_bf16_f32 v84, v83, v84
	s_waitcnt lgkmcnt(4)
	v_cvt_pk_bf16_f32 v85, v85, v86
	s_waitcnt lgkmcnt(2)
	v_cvt_pk_bf16_f32 v86, v87, v88
	s_waitcnt lgkmcnt(0)
	v_cvt_pk_bf16_f32 v87, v89, v90
	global_store_dwordx4 v[58:59], v[84:87], off nt
	s_barrier
	s_cbranch_vccz .LBB0_132

; __device__ __forceinline__ unsigned pk2(float lo, float hi) { unsigned r; asm("v_cvt_pk_bf16_f32 %0, %1, %2" : "=v"(r) : "v"(lo), "v"(hi)); return r; }
; __device__ __forceinline__ int ab_phys(int n) {
;     if (n < 1024) { const int hd = n >> 6, jj = n & 63; return (hd >> 2) * 256 + (jj >> 5) * 128 + (hd & 3) * 32 + (jj & 31); }
;     if (n < 1152) { const int nn = n - 1024, hh = nn >> 6, jj = nn & 63; return 1024 + (jj >> 5) * 128 + hh * 32 + (jj & 31); }
;     if (n < 1280) { const int vv = n - 1152; return 1024 + (vv >> 6) * 128 + 64 + (vv & 63); }
;     if (n < 2304) { const int base = n < 1792 ? 1280 : 1792, nn = n - base, h = nn >> 7, jj = nn & 127; return base + (h >> 1) * 256 + (jj >> 6) * 128 + (h & 1) * 64 + (jj & 63); }
;     return n;
; template <int TN, class DstFn>
; __device__ __forceinline__ void convert_T(const Ctx& c, const float* src, int nmat, int K, int N, DstFn dstfn) {
;     ...
;         { const int ch = c.tid & 7, nb = c.tid >> 3;
; #pragma unroll
;           for (int j = 0; j < TN / 64; ++j) { const int n = nb + 64 * j;
;               bf16_t* d = dstfn(m, nt * TN + n) + kt * 64 + ch * 8; u32x4 w;
; #pragma unroll
;               for (int e = 0; e < 4; ++e) w[e] = pk2(tile[(ch * 8 + 2 * e) * LDT + n], tile[(ch * 8 + 2 * e + 1) * LDT + n]);
;               *(u32x4*)d = w; } }
.LBB0_88:
	s_andn2_saveexec_b64 s[10:11], s[10:11]
	v_and_or_b32 v60, v60, s38, v71
	s_or_b64 exec, exec, s[10:11]
	s_mul_hi_i32 s11, s15, 0x880000
	s_mul_i32 s15, s15, 0x880000
	s_sext_i32_i16 s10, s39
	s_add_u32 s12, s19, s15
	s_addc_u32 s13, s24, s11
	s_lshl_b32 s10, s10, 6
	s_ashr_i32 s11, s10, 31
	s_lshl_b64 s[10:11], s[10:11], 1
	ds_read_b32 v83, v62
	ds_read_b32 v84, v62 offset:1028
	ds_read_b32 v85, v62 offset:2056
	ds_read_b32 v86, v62 offset:3084
	ds_read_b32 v87, v62 offset:4112
	ds_read_b32 v88, v62 offset:5140
	ds_read_b32 v89, v62 offset:6168
	ds_read_b32 v90, v62 offset:7196
	s_add_u32 s10, s12, s10
	s_addc_u32 s11, s13, s11
	v_ashrrev_i32_e32 v61, 31, v60
	v_lshl_add_u64 v[58:59], s[10:11], 0, v[36:37]
	v_lshlrev_b64 v[60:61], 11, v[60:61]
	v_lshl_add_u64 v[60:61], v[58:59], 0, v[60:61]
	s_waitcnt lgkmcnt(6)
	v_cvt_pk_bf16_f32 v84, v83, v84
	s_waitcnt lgkmcnt(4)
	v_cvt_pk_bf16_f32 v85, v85, v86
	s_waitcnt lgkmcnt(2)
	v_cvt_pk_bf16_f32 v86, v87, v88
	s_waitcnt lgkmcnt(0)
	v_cvt_pk_bf16_f32 v87, v89, v90
	global_store_dwordx4 v[60:61], v[84:87], off nt
	v_add_u32_e32 v60, s7, v64
	v_cmp_lt_i32_e32 vcc, s27, v60
	s_and_saveexec_b64 s[10:11], vcc
	s_xor_b64 s[10:11], exec, s[10:11]
	s_cbranch_execz .LBB0_102
	v_cmp_lt_u32_e32 vcc, s34, v60
	s_and_saveexec_b64 s[12:13], vcc
	s_xor_b64 s[12:13], exec, s[12:13]
	s_cbranch_execz .LBB0_99
	v_cmp_lt_u32_e32 vcc, s35, v60
	s_and_saveexec_b64 s[20:21], vcc
	s_xor_b64 s[20:21], exec, s[20:21]
	s_cbranch_execz .LBB0_96
	v_cmp_gt_u32_e32 vcc, s36, v60
	s_and_saveexec_b64 s[22:23], vcc
	v_cmp_gt_u32_e32 vcc, s37, v60
	s_nop 1
	v_cndmask_b32_e32 v61, v80, v81, vcc
	v_sub_u32_e32 v83, v60, v61
	v_and_b32_e32 v83, 0xffffff00, v83
	v_lshlrev_b32_e32 v60, 1, v60
	v_add_u32_e32 v61, v83, v61
	v_and_b32_e32 v60, 0x80, v60
	v_or3_b32 v60, v61, v60, v65
	s_or_b64 exec, exec, s[22:23]

; __device__ __forceinline__ unsigned pk2(float lo, float hi) { unsigned r; asm("v_cvt_pk_bf16_f32 %0, %1, %2" : "=v"(r) : "v"(lo), "v"(hi)); return r; }
; __device__ __forceinline__ int ab_phys(int n) {
;     if (n < 1024) { const int hd = n >> 6, jj = n & 63; return (hd >> 2) * 256 + (jj >> 5) * 128 + (hd & 3) * 32 + (jj & 31); }
;     if (n < 1152) { const int nn = n - 1024, hh = nn >> 6, jj = nn & 63; return 1024 + (jj >> 5) * 128 + hh * 32 + (jj & 31); }
;     if (n < 1280) { const int vv = n - 1152; return 1024 + (vv >> 6) * 128 + 64 + (vv & 63); }
;     if (n < 2304) { const int base = n < 1792 ? 1280 : 1792, nn = n - base, h = nn >> 7, jj = nn & 127; return base + (h >> 1) * 256 + (jj >> 6) * 128 + (h & 1) * 64 + (jj & 63); }
;     return n;
; template <int TN, class DstFn>
; __device__ __forceinline__ void convert_T(const Ctx& c, const float* src, int nmat, int K, int N, DstFn dstfn) {
;     ...
;         { const int ch = c.tid & 7, nb = c.tid >> 3;
; #pragma unroll
;           for (int j = 0; j < TN / 64; ++j) { const int n = nb + 64 * j;
;               bf16_t* d = dstfn(m, nt * TN + n) + kt * 64 + ch * 8; u32x4 w;
; #pragma unroll
;               for (int e = 0; e < 4; ++e) w[e] = pk2(tile[(ch * 8 + 2 * e) * LDT + n], tile[(ch * 8 + 2 * e + 1) * LDT + n]);
;               *(u32x4*)d = w; } }
.LBB0_102:
	s_andn2_saveexec_b64 s[10:11], s[10:11]
	v_and_or_b32 v60, v60, s38, v72
	s_or_b64 exec, exec, s[10:11]
	ds_read_b32 v83, v62 offset:256
	ds_read_b32 v84, v62 offset:1284
	ds_read_b32 v85, v62 offset:2312
	ds_read_b32 v86, v62 offset:3340
	ds_read_b32 v87, v62 offset:4368
	ds_read_b32 v88, v62 offset:5396
	ds_read_b32 v89, v62 offset:6424
	ds_read_b32 v90, v62 offset:7452
	v_ashrrev_i32_e32 v61, 31, v60
	v_lshlrev_b64 v[60:61], 11, v[60:61]
	v_lshl_add_u64 v[60:61], v[58:59], 0, v[60:61]
	s_waitcnt lgkmcnt(6)
	v_cvt_pk_bf16_f32 v84, v83, v84
	s_waitcnt lgkmcnt(4)
	v_cvt_pk_bf16_f32 v85, v85, v86
	s_waitcnt lgkmcnt(2)
	v_cvt_pk_bf16_f32 v86, v87, v88
	s_waitcnt lgkmcnt(0)
	v_cvt_pk_bf16_f32 v87, v89, v90
	global_store_dwordx4 v[60:61], v[84:87], off nt
	v_add_u32_e32 v60, s7, v66
	v_cmp_lt_i32_e32 vcc, s27, v60
	s_and_saveexec_b64 s[10:11], vcc
	s_xor_b64 s[10:11], exec, s[10:11]
	s_cbranch_execz .LBB0_116
	v_cmp_lt_u32_e32 vcc, s34, v60
	s_and_saveexec_b64 s[12:13], vcc
	s_xor_b64 s[12:13], exec, s[12:13]
	s_cbranch_execz .LBB0_113
	v_cmp_lt_u32_e32 vcc, s35, v60
	s_and_saveexec_b64 s[20:21], vcc
	s_xor_b64 s[20:21], exec, s[20:21]
	s_cbranch_execz .LBB0_110
	v_cmp_gt_u32_e32 vcc, s36, v60
	s_and_saveexec_b64 s[22:23], vcc
	v_cmp_gt_u32_e32 vcc, s37, v60
	s_nop 1
	v_cndmask_b32_e32 v61, v80, v81, vcc
	v_sub_u32_e32 v83, v60, v61
	v_and_b32_e32 v83, 0xffffff00, v83
	v_lshlrev_b32_e32 v60, 1, v60
	v_add_u32_e32 v61, v83, v61
	v_and_b32_e32 v60, 0x80, v60
	v_or3_b32 v60, v61, v60, v67
	s_or_b64 exec, exec, s[22:23]

; __device__ __forceinline__ unsigned pk2(float lo, float hi) { unsigned r; asm("v_cvt_pk_bf16_f32 %0, %1, %2" : "=v"(r) : "v"(lo), "v"(hi)); return r; }
; __device__ __forceinline__ int ab_phys(int n) {
;     if (n < 1024) { const int hd = n >> 6, jj = n & 63; return (hd >> 2) * 256 + (jj >> 5) * 128 + (hd & 3) * 32 + (jj & 31); }
;     if (n < 1152) { const int nn = n - 1024, hh = nn >> 6, jj = nn & 63; return 1024 + (jj >> 5) * 128 + hh * 32 + (jj & 31); }
;     if (n < 1280) { const int vv = n - 1152; return 1024 + (vv >> 6) * 128 + 64 + (vv & 63); }
;     if (n < 2304) { const int base = n < 1792 ? 1280 : 1792, nn = n - base, h = nn >> 7, jj = nn & 127; return base + (h >> 1) * 256 + (jj >> 6) * 128 + (h & 1) * 64 + (jj & 63); }
;     return n;
; template <int TN, class DstFn>
; __device__ __forceinline__ void convert_T(const Ctx& c, const float* src, int nmat, int K, int N, DstFn dstfn) {
;     ...
;         { const int ch = c.tid & 7, nb = c.tid >> 3;
; #pragma unroll
;           for (int j = 0; j < TN / 64; ++j) { const int n = nb + 64 * j;
;               bf16_t* d = dstfn(m, nt * TN + n) + kt * 64 + ch * 8; u32x4 w;
; #pragma unroll
;               for (int e = 0; e < 4; ++e) w[e] = pk2(tile[(ch * 8 + 2 * e) * LDT + n], tile[(ch * 8 + 2 * e + 1) * LDT + n]);
;               *(u32x4*)d = w; } }
.LBB0_116:
	s_andn2_saveexec_b64 s[10:11], s[10:11]
	v_and_or_b32 v60, v60, s38, v73
	s_or_b64 exec, exec, s[10:11]
	ds_read_b32 v83, v62 offset:512
	ds_read_b32 v84, v62 offset:1540
	ds_read_b32 v85, v62 offset:2568
	ds_read_b32 v86, v62 offset:3596
	ds_read_b32 v87, v62 offset:4624
	ds_read_b32 v88, v62 offset:5652
	ds_read_b32 v89, v62 offset:6680
	ds_read_b32 v90, v62 offset:7708
	v_ashrrev_i32_e32 v61, 31, v60
	v_lshlrev_b64 v[60:61], 11, v[60:61]
	v_lshl_add_u64 v[60:61], v[58:59], 0, v[60:61]
	s_waitcnt lgkmcnt(6)
	v_cvt_pk_bf16_f32 v84, v83, v84
	s_waitcnt lgkmcnt(4)
	v_cvt_pk_bf16_f32 v85, v85, v86
	s_waitcnt lgkmcnt(2)
	v_cvt_pk_bf16_f32 v86, v87, v88
	s_waitcnt lgkmcnt(0)
	v_cvt_pk_bf16_f32 v87, v89, v90
	global_store_dwordx4 v[60:61], v[84:87], off nt
	v_add_u32_e32 v60, s7, v68
	v_cmp_lt_i32_e32 vcc, s27, v60
	s_and_saveexec_b64 s[10:11], vcc
	s_xor_b64 s[10:11], exec, s[10:11]
	s_cbranch_execz .LBB0_130
	v_cmp_lt_u32_e32 vcc, s34, v60
	s_and_saveexec_b64 s[12:13], vcc
	s_xor_b64 s[12:13], exec, s[12:13]
	s_cbranch_execz .LBB0_127
	v_cmp_lt_u32_e32 vcc, s35, v60
	s_and_saveexec_b64 s[20:21], vcc
	s_xor_b64 s[20:21], exec, s[20:21]
	s_cbranch_execz .LBB0_124
	v_cmp_gt_u32_e32 vcc, s36, v60
	s_and_saveexec_b64 s[22:23], vcc
	v_cmp_gt_u32_e32 vcc, s37, v60
	s_nop 1
	v_cndmask_b32_e32 v61, v80, v81, vcc
	v_sub_u32_e32 v83, v60, v61
	v_and_b32_e32 v83, 0xffffff00, v83
	v_lshlrev_b32_e32 v60, 1, v60
	v_add_u32_e32 v61, v83, v61
	v_and_b32_e32 v60, 0x80, v60
	v_or3_b32 v60, v61, v60, v69
	s_or_b64 exec, exec, s[22:23]

; __device__ __forceinline__ unsigned pk2(float lo, float hi) { unsigned r; asm("v_cvt_pk_bf16_f32 %0, %1, %2" : "=v"(r) : "v"(lo), "v"(hi)); return r; }
;     __device__ __forceinline__ const float* inp(int k) const { return (const float*)in[k]; }
; template <int TN, class DstFn>
; __device__ __forceinline__ void convert_T(const Ctx& c, const float* src, int nmat, int K, int N, DstFn dstfn) {
;     ...
;     for (long tix = c.bid; tix < ntiles; tix += c.G) {
;         const int m = (int)(tix / (tk * tn)); const int rem = (int)(tix % (tk * tn)); const int kt = rem / tn, nt = rem % tn;
; #pragma unroll
;         for (int i = 0; i < NI; ++i) { const int k = c.tid / TPR + KPI * i, n4 = (c.tid % TPR) * 4;
;             tile[k * LDT + n4 + 0] = v[i][0]; tile[k * LDT + n4 + 1] = v[i][1]; tile[k * LDT + n4 + 2] = v[i][2]; tile[k * LDT + n4 + 3] = v[i][3]; }
;         if (tix + c.G < ntiles) issue(tix + c.G);
;         __syncthreads();
;         { const int ch = c.tid & 7, nb = c.tid >> 3;
; #pragma unroll
;           for (int j = 0; j < TN / 64; ++j) { const int n = nb + 64 * j;
;               bf16_t* d = dstfn(m, nt * TN + n) + kt * 64 + ch * 8; u32x4 w;
; #pragma unroll
;               for (int e = 0; e < 4; ++e) w[e] = pk2(tile[(ch * 8 + 2 * e) * LDT + n], tile[(ch * 8 + 2 * e + 1) * LDT + n]);
;               *(u32x4*)d = w; } }
; __device__ __forceinline__ void phase_convert(const Ctx& c) {
;     ...
;     { bf16_t* d = (bf16_t*)(ws + WS_WABOUT); convert_T<256>(c, c.inp(4), 2, AB_OUT, D, [=](int m, int n) { return d + (size_t)m * D * AB_OUT + (size_t)n * AB_OUT; }); }
.LBB0_134:
	s_ashr_i32 s7, s11, 31
	s_lshr_b32 s7, s7, 25
	s_add_u32 s20, s10, s7
	s_addc_u32 s21, s11, 0
	s_ashr_i64 s[20:21], s[20:21], 7
	s_lshl_b32 s7, s20, 7
	s_sub_i32 s7, s10, s7
	s_bfe_i32 s10, s7, 0x80000
	s_bfe_u32 s10, s10, 0x2000d
	s_add_i32 s10, s7, s10
	s_bfe_i32 s11, s10, 0x80000
	s_and_b32 s10, s10, 0xfc
	s_sub_i32 s7, s7, s10
	s_sext_i32_i8 s21, s7
	s_mov_b32 s7, s20
	s_sext_i32_i16 s15, s11
	s_ashr_i64 s[10:11], s[6:7], 10
	s_add_u32 s7, s12, s10
	s_addc_u32 s20, s13, s11
	s_lshl_b32 s10, s15, 4
	s_andn2_b32 s10, s10, 63
	s_ashr_i32 s11, s10, 31
	v_lshl_add_u32 v66, s21, 8, v32
	s_lshl_b64 s[10:11], s[10:11], 1
	v_ashrrev_i32_e32 v67, 31, v66
	v_add_u32_e32 v59, 4, v33
	v_add_u32_e32 v61, 8, v33
	v_add_u32_e32 v62, 12, v33
	s_waitcnt lgkmcnt(0)
	s_barrier
	s_add_u32 s10, s7, s10
	v_lshlrev_b64 v[68:69], 12, v[66:67]
	ds_read2st64_b32 v[70:71], v33 offset1:1
	ds_read2st64_b32 v[72:73], v59 offset0:4 offset1:5
	ds_read2st64_b32 v[74:75], v61 offset0:8 offset1:9
	ds_read2st64_b32 v[80:81], v62 offset0:12 offset1:13
	ds_read2st64_b32 v[82:83], v33 offset0:2 offset1:3
	ds_read2st64_b32 v[84:85], v59 offset0:6 offset1:7
	ds_read2st64_b32 v[86:87], v61 offset0:10 offset1:11
	ds_read2st64_b32 v[88:89], v62 offset0:14 offset1:15
	v_add_u32_e32 v59, 16, v33
	v_add_u32_e32 v62, 20, v33
	v_add_u32_e32 v63, 24, v33
	v_add_u32_e32 v67, 28, v33
	s_addc_u32 s11, s20, s11
	ds_read2st64_b32 v[90:91], v59 offset0:16 offset1:17
	ds_read2st64_b32 v[92:93], v62 offset0:20 offset1:21
	ds_read2st64_b32 v[94:95], v63 offset0:24 offset1:25
	ds_read2st64_b32 v[96:97], v67 offset0:28 offset1:29
	ds_read2st64_b32 v[98:99], v59 offset0:18 offset1:19
	ds_read2st64_b32 v[100:101], v62 offset0:22 offset1:23
	v_lshl_add_u64 v[64:65], s[10:11], 0, v[54:55]
	s_waitcnt lgkmcnt(12)
	v_cvt_pk_bf16_f32 v60, v70, v72
	v_lshl_add_u64 v[68:69], v[64:65], 0, v[68:69]
	s_waitcnt lgkmcnt(10)
	v_cvt_pk_bf16_f32 v61, v74, v80
	s_waitcnt lgkmcnt(4)
	v_cvt_pk_bf16_f32 v62, v90, v92
	ds_read2st64_b32 v[102:103], v63 offset0:26 offset1:27
	ds_read2st64_b32 v[104:105], v67 offset0:30 offset1:31
	s_waitcnt lgkmcnt(4)
	v_cvt_pk_bf16_f32 v63, v94, v96
	global_store_dwordx4 v[68:69], v[60:63], off nt
	s_andn2_b64 vcc, exec, s[2:3]
	s_mov_b64 s[10:11], s[8:9]
	v_add_u32_e32 v60, 64, v66
	v_ashrrev_i32_e32 v61, 31, v60
	v_lshlrev_b64 v[68:69], 12, v[60:61]
	v_cvt_pk_bf16_f32 v60, v71, v73
	v_lshl_add_u64 v[68:69], v[64:65], 0, v[68:69]
	v_cvt_pk_bf16_f32 v61, v75, v81
	v_cvt_pk_bf16_f32 v62, v91, v93
	v_cvt_pk_bf16_f32 v63, v95, v97
	global_store_dwordx4 v[68:69], v[60:63], off nt
	s_nop 1
	v_add_u32_e32 v60, 0x80, v66
	v_ashrrev_i32_e32 v61, 31, v60
	v_lshlrev_b64 v[68:69], 12, v[60:61]
	v_cvt_pk_bf16_f32 v60, v82, v84
	v_lshl_add_u64 v[68:69], v[64:65], 0, v[68:69]
	v_cvt_pk_bf16_f32 v61, v86, v88
	s_waitcnt lgkmcnt(2)
	v_cvt_pk_bf16_f32 v62, v98, v100
	s_waitcnt lgkmcnt(0)
	v_cvt_pk_bf16_f32 v63, v102, v104
	global_store_dwordx4 v[68:69], v[60:63], off nt
	s_nop 1
	v_add_u32_e32 v60, 0xc0, v66
	v_ashrrev_i32_e32 v61, 31, v60
	v_lshlrev_b64 v[66:67], 12, v[60:61]
	v_lshl_add_u64 v[64:65], v[64:65], 0, v[66:67]
	v_cvt_pk_bf16_f32 v60, v83, v85
	v_cvt_pk_bf16_f32 v61, v87, v89
	v_cvt_pk_bf16_f32 v62, v99, v101
	v_cvt_pk_bf16_f32 v63, v103, v105
	global_store_dwordx4 v[64:65], v[60:63], off nt
	s_barrier
	s_cbranch_vccz .LBB0_137

; __device__ __forceinline__ unsigned pk2(float lo, float hi) { unsigned r; asm("v_cvt_pk_bf16_f32 %0, %1, %2" : "=v"(r) : "v"(lo), "v"(hi)); return r; }
;     __device__ __forceinline__ const float* inp(int k) const { return (const float*)in[k]; }
; template <int TN, class DstFn>
; __device__ __forceinline__ void convert_T(const Ctx& c, const float* src, int nmat, int K, int N, DstFn dstfn) {
;     ...
;     for (long tix = c.bid; tix < ntiles; tix += c.G) {
;         const int m = (int)(tix / (tk * tn)); const int rem = (int)(tix % (tk * tn)); const int kt = rem / tn, nt = rem % tn;
; #pragma unroll
;         for (int i = 0; i < NI; ++i) { const int k = c.tid / TPR + KPI * i, n4 = (c.tid % TPR) * 4;
;             tile[k * LDT + n4 + 0] = v[i][0]; tile[k * LDT + n4 + 1] = v[i][1]; tile[k * LDT + n4 + 2] = v[i][2]; tile[k * LDT + n4 + 3] = v[i][3]; }
;         if (tix + c.G < ntiles) issue(tix + c.G);
;         __syncthreads();
;         { const int ch = c.tid & 7, nb = c.tid >> 3;
; #pragma unroll
;           for (int j = 0; j < TN / 64; ++j) { const int n = nb + 64 * j;
;               bf16_t* d = dstfn(m, nt * TN + n) + kt * 64 + ch * 8; u32x4 w;
; #pragma unroll
;               for (int e = 0; e < 4; ++e) w[e] = pk2(tile[(ch * 8 + 2 * e) * LDT + n], tile[(ch * 8 + 2 * e + 1) * LDT + n]);
;               *(u32x4*)d = w; } }
; __device__ __forceinline__ void phase_convert(const Ctx& c) {
;     ...
;     { bf16_t* d = (bf16_t*)(ws + WS_WCDIN);  convert_T<256>(c, c.inp(6), 2, D, CD_IN, [=](int m, int n) { return d + (size_t)m * CD_IN * D + (size_t)n * D; }); }
.LBB0_139:
	s_mul_i32 s22, s11, 0x38e38e39
	s_mul_hi_u32 s23, s10, 0x38e38e39
	s_mul_hi_u32 s21, s11, 0x38e38e39
	s_add_u32 s22, s22, s23
	s_mul_i32 s15, s10, 0xe38e38e
	s_addc_u32 s21, s21, 0
	s_mul_hi_u32 s7, s10, 0xe38e38e
	s_add_u32 s15, s15, s22
	s_addc_u32 s7, s7, 0
	s_add_u32 s7, s21, s7
	s_addc_u32 s15, 0, 0
	s_mul_i32 s22, s11, 0xe38e38e
	s_mul_hi_u32 s21, s11, 0xe38e38e
	s_add_u32 s7, s22, s7
	s_addc_u32 s15, s21, s15
	s_ashr_i32 s11, s11, 31
	s_mul_i32 s21, s11, 0xe38e38e
	s_mul_hi_u32 s22, s11, 0x38e38e39
	s_add_i32 s21, s22, s21
	s_mul_i32 s11, s11, 0x38e38e39
	s_add_i32 s21, s21, s11
	s_add_u32 s22, s7, s11
	s_addc_u32 s23, s15, s21
	s_lshr_b32 s7, s23, 31
	s_lshr_b64 s[22:23], s[22:23], 4
	s_add_i32 s7, s22, s7
	s_mul_i32 s11, s7, 0xfffffee0
	s_add_i32 s10, s10, s11
	s_sext_i32_i16 s11, s10
	s_mulk_i32 s11, 0xe39
	s_lshr_b32 s15, s11, 31
	s_lshr_b32 s11, s11, 16
	s_add_i32 s11, s11, s15
	s_mul_i32 s15, s11, 18
	s_sub_i32 s10, s10, s15
	s_sext_i32_i16 s15, s10
	s_mul_hi_i32 s10, s7, 0x900000
	s_mul_i32 s7, s7, 0x900000
	s_sext_i32_i16 s11, s11
	s_add_u32 s7, s13, s7
	s_addc_u32 s21, s19, s10
	s_lshl_b32 s10, s11, 6
	s_ashr_i32 s11, s10, 31
	v_lshl_add_u32 v66, s15, 8, v32
	s_lshl_b64 s[10:11], s[10:11], 1
	v_ashrrev_i32_e32 v67, 31, v66
	v_add_u32_e32 v59, 4, v33
	v_add_u32_e32 v61, 8, v33
	v_add_u32_e32 v62, 12, v33
	s_waitcnt lgkmcnt(0)
	s_barrier
	s_add_u32 s10, s7, s10
	v_lshlrev_b64 v[68:69], 11, v[66:67]
	ds_read2st64_b32 v[70:71], v33 offset1:1
	ds_read2st64_b32 v[72:73], v59 offset0:4 offset1:5
	ds_read2st64_b32 v[74:75], v61 offset0:8 offset1:9
	ds_read2st64_b32 v[80:81], v62 offset0:12 offset1:13
	ds_read2st64_b32 v[82:83], v33 offset0:2 offset1:3
	ds_read2st64_b32 v[84:85], v59 offset0:6 offset1:7
	ds_read2st64_b32 v[86:87], v61 offset0:10 offset1:11
	ds_read2st64_b32 v[88:89], v62 offset0:14 offset1:15
	v_add_u32_e32 v59, 16, v33
	v_add_u32_e32 v62, 20, v33
	v_add_u32_e32 v63, 24, v33
	v_add_u32_e32 v67, 28, v33
	s_addc_u32 s11, s21, s11
	ds_read2st64_b32 v[90:91], v59 offset0:16 offset1:17
	ds_read2st64_b32 v[92:93], v62 offset0:20 offset1:21
	ds_read2st64_b32 v[94:95], v63 offset0:24 offset1:25
	ds_read2st64_b32 v[96:97], v67 offset0:28 offset1:29
	ds_read2st64_b32 v[98:99], v59 offset0:18 offset1:19
	ds_read2st64_b32 v[100:101], v62 offset0:22 offset1:23
	v_lshl_add_u64 v[64:65], s[10:11], 0, v[54:55]
	s_waitcnt lgkmcnt(12)
	v_cvt_pk_bf16_f32 v60, v70, v72
	v_lshl_add_u64 v[68:69], v[64:65], 0, v[68:69]
	s_waitcnt lgkmcnt(10)
	v_cvt_pk_bf16_f32 v61, v74, v80
	s_waitcnt lgkmcnt(4)
	v_cvt_pk_bf16_f32 v62, v90, v92
	ds_read2st64_b32 v[102:103], v63 offset0:26 offset1:27
	ds_read2st64_b32 v[104:105], v67 offset0:30 offset1:31
	s_waitcnt lgkmcnt(4)
	v_cvt_pk_bf16_f32 v63, v94, v96
	global_store_dwordx4 v[68:69], v[60:63], off nt
	s_andn2_b64 vcc, exec, s[2:3]
	s_mov_b64 s[10:11], s[8:9]
	v_add_u32_e32 v60, 64, v66
	v_ashrrev_i32_e32 v61, 31, v60
	v_lshlrev_b64 v[68:69], 11, v[60:61]
	v_cvt_pk_bf16_f32 v60, v71, v73
	v_lshl_add_u64 v[68:69], v[64:65], 0, v[68:69]
	v_cvt_pk_bf16_f32 v61, v75, v81
	v_cvt_pk_bf16_f32 v62, v91, v93
	v_cvt_pk_bf16_f32 v63, v95, v97
	global_store_dwordx4 v[68:69], v[60:63], off nt
	s_nop 1
	v_add_u32_e32 v60, 0x80, v66
	v_ashrrev_i32_e32 v61, 31, v60
	v_lshlrev_b64 v[68:69], 11, v[60:61]
	v_cvt_pk_bf16_f32 v60, v82, v84
	v_lshl_add_u64 v[68:69], v[64:65], 0, v[68:69]
	v_cvt_pk_bf16_f32 v61, v86, v88
	s_waitcnt lgkmcnt(2)
	v_cvt_pk_bf16_f32 v62, v98, v100
	s_waitcnt lgkmcnt(0)
	v_cvt_pk_bf16_f32 v63, v102, v104
	global_store_dwordx4 v[68:69], v[60:63], off nt
	s_nop 1
	v_add_u32_e32 v60, 0xc0, v66
	v_ashrrev_i32_e32 v61, 31, v60
	v_lshlrev_b64 v[66:67], 11, v[60:61]
	v_lshl_add_u64 v[64:65], v[64:65], 0, v[66:67]
	v_cvt_pk_bf16_f32 v60, v83, v85
	v_cvt_pk_bf16_f32 v61, v87, v89
	v_cvt_pk_bf16_f32 v62, v99, v101
	v_cvt_pk_bf16_f32 v63, v103, v105
	global_store_dwordx4 v[64:65], v[60:63], off nt
	s_barrier
	s_cbranch_vccz .LBB0_142

; __device__ __forceinline__ unsigned pk2(float lo, float hi) { unsigned r; asm("v_cvt_pk_bf16_f32 %0, %1, %2" : "=v"(r) : "v"(lo), "v"(hi)); return r; }
;     __device__ __forceinline__ const float* inp(int k) const { return (const float*)in[k]; }
; template <int TN, class DstFn>
; __device__ __forceinline__ void convert_T(const Ctx& c, const float* src, int nmat, int K, int N, DstFn dstfn) {
;     ...
;     for (long tix = c.bid; tix < ntiles; tix += c.G) {
;         const int m = (int)(tix / (tk * tn)); const int rem = (int)(tix % (tk * tn)); const int kt = rem / tn, nt = rem % tn;
; #pragma unroll
;         for (int i = 0; i < NI; ++i) { const int k = c.tid / TPR + KPI * i, n4 = (c.tid % TPR) * 4;
;             tile[k * LDT + n4 + 0] = v[i][0]; tile[k * LDT + n4 + 1] = v[i][1]; tile[k * LDT + n4 + 2] = v[i][2]; tile[k * LDT + n4 + 3] = v[i][3]; }
;         if (tix + c.G < ntiles) issue(tix + c.G);
;         __syncthreads();
;         { const int ch = c.tid & 7, nb = c.tid >> 3;
; #pragma unroll
;           for (int j = 0; j < TN / 64; ++j) { const int n = nb + 64 * j;
;               bf16_t* d = dstfn(m, nt * TN + n) + kt * 64 + ch * 8; u32x4 w;
; #pragma unroll
;               for (int e = 0; e < 4; ++e) w[e] = pk2(tile[(ch * 8 + 2 * e) * LDT + n], tile[(ch * 8 + 2 * e + 1) * LDT + n]);
;               *(u32x4*)d = w; } }
; __device__ __forceinline__ void phase_convert(const Ctx& c) {
;     ...
;     { bf16_t* d = (bf16_t*)(ws + WS_WCDOUT); convert_T<256>(c, c.inp(17), 2, CD_OUT, D, [=](int m, int n) { return d + (size_t)m * D * CD_OUT + (size_t)n * CD_OUT; }); }
.LBB0_144:
	s_mul_i32 s21, s9, 0x38e38e39
	s_mul_hi_u32 s22, s8, 0x38e38e39
	s_mul_hi_u32 s20, s9, 0x38e38e39
	s_add_u32 s21, s21, s22
	s_mul_i32 s19, s8, 0xe38e38e
	s_addc_u32 s20, s20, 0
	s_mul_hi_u32 s15, s8, 0xe38e38e
	s_add_u32 s19, s19, s21
	s_addc_u32 s15, s15, 0
	s_add_u32 s15, s20, s15
	s_addc_u32 s19, 0, 0
	s_mul_i32 s21, s9, 0xe38e38e
	s_mul_hi_u32 s20, s9, 0xe38e38e
	s_add_u32 s15, s21, s15
	s_addc_u32 s19, s20, s19
	s_ashr_i32 s9, s9, 31
	s_mul_i32 s20, s9, 0xe38e38e
	s_mul_hi_u32 s21, s9, 0x38e38e39
	s_add_i32 s20, s21, s20
	s_mul_i32 s9, s9, 0x38e38e39
	s_add_i32 s21, s20, s9
	s_add_u32 s20, s15, s9
	s_addc_u32 s21, s19, s21
	s_lshr_b32 s9, s21, 31
	s_lshr_b64 s[20:21], s[20:21], 3
	s_add_i32 s9, s20, s9
	s_mul_i32 s15, s9, 0xffffff70
	s_add_i32 s8, s8, s15
	s_sext_i32_i16 s15, s8
	s_bfe_u32 s15, s15, 0x2001d
	s_add_i32 s15, s8, s15
	s_sext_i32_i16 s19, s15
	s_and_b32 s15, s15, 0xfffc
	s_sub_i32 s8, s8, s15
	s_sext_i32_i16 s15, s8
	s_mul_hi_i32 s8, s9, 0x480000
	s_mul_i32 s9, s9, 0x480000
	s_add_u32 s20, s10, s9
	s_addc_u32 s21, s11, s8
	s_lshl_b32 s8, s19, 4
	s_andn2_b32 s8, s8, 63
	s_ashr_i32 s9, s8, 31
	v_add_u32_e32 v60, 4, v33
	s_waitcnt lgkmcnt(0)
	s_barrier
	s_lshl_b64 s[8:9], s[8:9], 1
	ds_read2st64_b32 v[66:67], v33 offset1:1
	ds_read2st64_b32 v[68:69], v60 offset0:4 offset1:5
	v_add_u32_e32 v61, 8, v33
	v_add_u32_e32 v62, 12, v33
	s_add_u32 s8, s20, s8
	ds_read2st64_b32 v[70:71], v61 offset0:8 offset1:9
	ds_read2st64_b32 v[72:73], v62 offset0:12 offset1:13
	ds_read2st64_b32 v[74:75], v33 offset0:2 offset1:3
	ds_read2st64_b32 v[80:81], v60 offset0:6 offset1:7
	s_waitcnt lgkmcnt(4)
	v_cvt_pk_bf16_f32 v60, v66, v68
	ds_read2st64_b32 v[82:83], v61 offset0:10 offset1:11
	ds_read2st64_b32 v[84:85], v62 offset0:14 offset1:15
	v_add_u32_e32 v62, 16, v33
	v_add_u32_e32 v63, 20, v33
	v_add_u32_e32 v66, 24, v33
	v_add_u32_e32 v68, 28, v33
	s_addc_u32 s9, s21, s9
	ds_read2st64_b32 v[86:87], v62 offset0:16 offset1:17
	ds_read2st64_b32 v[88:89], v63 offset0:20 offset1:21
	ds_read2st64_b32 v[90:91], v66 offset0:24 offset1:25
	ds_read2st64_b32 v[92:93], v68 offset0:28 offset1:29
	ds_read2st64_b32 v[94:95], v62 offset0:18 offset1:19
	ds_read2st64_b32 v[96:97], v63 offset0:22 offset1:23
	v_lshl_add_u64 v[64:65], s[8:9], 0, v[54:55]
	v_lshl_add_u32 v59, s15, 8, v32
	ds_read2st64_b32 v[98:99], v66 offset0:26 offset1:27
	ds_read2st64_b32 v[100:101], v68 offset0:30 offset1:31
	v_mad_i64_i32 v[102:103], s[8:9], v59, s13, v[64:65]
	v_add_u32_e32 v66, 64, v59
	s_waitcnt lgkmcnt(12)
	v_cvt_pk_bf16_f32 v61, v70, v72
	s_waitcnt lgkmcnt(6)
	v_cvt_pk_bf16_f32 v62, v86, v88
	s_waitcnt lgkmcnt(4)
	v_cvt_pk_bf16_f32 v63, v90, v92
	global_store_dwordx4 v[102:103], v[60:63], off nt
	s_andn2_b64 vcc, exec, s[2:3]
	s_nop 0
	v_cvt_pk_bf16_f32 v60, v67, v69
	v_mad_i64_i32 v[66:67], s[8:9], v66, s13, v[64:65]
	v_cvt_pk_bf16_f32 v61, v71, v73
	v_cvt_pk_bf16_f32 v62, v87, v89
	v_cvt_pk_bf16_f32 v63, v91, v93
	global_store_dwordx4 v[66:67], v[60:63], off nt
	v_add_u32_e32 v66, 0x80, v59
	v_add_u32_e32 v59, 0xc0, v59
	v_mad_i64_i32 v[66:67], s[8:9], v66, s13, v[64:65]
	v_mad_i64_i32 v[64:65], s[8:9], v59, s13, v[64:65]
	v_cvt_pk_bf16_f32 v60, v74, v80
	v_cvt_pk_bf16_f32 v61, v82, v84
	s_waitcnt lgkmcnt(2)
	v_cvt_pk_bf16_f32 v62, v94, v96
	s_waitcnt lgkmcnt(0)
	v_cvt_pk_bf16_f32 v63, v98, v100
	s_mov_b64 s[8:9], s[6:7]
	global_store_dwordx4 v[66:67], v[60:63], off nt
	s_nop 1
	v_cvt_pk_bf16_f32 v60, v75, v81
	v_cvt_pk_bf16_f32 v61, v83, v85
	v_cvt_pk_bf16_f32 v62, v95, v97
	v_cvt_pk_bf16_f32 v63, v99, v101
	global_store_dwordx4 v[64:65], v[60:63], off nt
	s_barrier
	s_cbranch_vccz .LBB0_147

; __device__ __forceinline__ unsigned pk2(float lo, float hi) { unsigned r; asm("v_cvt_pk_bf16_f32 %0, %1, %2" : "=v"(r) : "v"(lo), "v"(hi)); return r; }
;     __device__ __forceinline__ const float* inp(int k) const { return (const float*)in[k]; }
; template <int TN, class DstFn>
; __device__ __forceinline__ void convert_T(const Ctx& c, const float* src, int nmat, int K, int N, DstFn dstfn) {
;     ...
;     for (long tix = c.bid; tix < ntiles; tix += c.G) {
;         const int m = (int)(tix / (tk * tn)); const int rem = (int)(tix % (tk * tn)); const int kt = rem / tn, nt = rem % tn;
; #pragma unroll
;         for (int i = 0; i < NI; ++i) { const int k = c.tid / TPR + KPI * i, n4 = (c.tid % TPR) * 4;
;             tile[k * LDT + n4 + 0] = v[i][0]; tile[k * LDT + n4 + 1] = v[i][1]; tile[k * LDT + n4 + 2] = v[i][2]; tile[k * LDT + n4 + 3] = v[i][3]; }
;         if (tix + c.G < ntiles) issue(tix + c.G);
;         __syncthreads();
;         { const int ch = c.tid & 7, nb = c.tid >> 3;
; #pragma unroll
;           for (int j = 0; j < TN / 64; ++j) { const int n = nb + 64 * j;
;               bf16_t* d = dstfn(m, nt * TN + n) + kt * 64 + ch * 8; u32x4 w;
; #pragma unroll
;               for (int e = 0; e < 4; ++e) w[e] = pk2(tile[(ch * 8 + 2 * e) * LDT + n], tile[(ch * 8 + 2 * e + 1) * LDT + n]);
;               *(u32x4*)d = w; } }
; __device__ __forceinline__ void phase_convert(const Ctx& c) {
;     ...
;     { bf16_t* d = (bf16_t*)(ws + WS_WRT);    convert_T<128>(c, c.inp(21), 4, D, NE, [=](int m, int n) { return d + (size_t)m * 256 * D + (size_t)n * D; }); }
.LBB0_149:
	s_ashr_i32 s5, s13, 31
	s_lshr_b32 s5, s5, 28
	s_add_u32 s12, s12, s5
	s_addc_u32 s13, s13, 0
	s_ashr_i64 s[12:13], s[12:13], 4
	s_mov_b32 s5, s12
	s_ashr_i64 s[20:21], s[4:5], 13
	s_add_u32 s5, s19, s20
	s_addc_u32 s20, s22, s21
	s_lshl_b32 s12, s12, 10
	s_sub_i32 s12, s25, s12
	s_waitcnt lgkmcnt(0)
	s_barrier
	s_ashr_i32 s13, s12, 31
	ds_read2st64_b32 v[48:49], v33 offset1:1
	ds_read2_b32 v[50:51], v33 offset0:129 offset1:193
	v_add_u32_e32 v43, 8, v33
	s_lshl_b64 s[12:13], s[12:13], 1
	ds_read2st64_b32 v[52:53], v43 offset0:4 offset1:5
	v_add_u32_e32 v43, 12, v33
	s_add_u32 s12, s5, s12
	ds_read2st64_b32 v[54:55], v43 offset0:6 offset1:7
	v_add_u32_e32 v43, 16, v33
	s_addc_u32 s13, s20, s13
	ds_read2st64_b32 v[56:57], v43 offset0:8 offset1:9
	v_add_u32_e32 v43, 20, v33
	ds_read2st64_b32 v[58:59], v43 offset0:10 offset1:11
	v_add_u32_e32 v43, 24, v33
	v_lshl_add_u64 v[64:65], s[12:13], 0, v[26:27]
	ds_read2st64_b32 v[60:61], v43 offset0:12 offset1:13
	v_add_u32_e32 v43, 28, v33
	s_waitcnt lgkmcnt(5)
	v_cvt_pk_bf16_f32 v44, v48, v50
	v_lshl_add_u64 v[66:67], v[64:65], 0, v[28:29]
	ds_read2st64_b32 v[62:63], v43 offset0:14 offset1:15
	s_waitcnt lgkmcnt(4)
	v_cvt_pk_bf16_f32 v45, v52, v54
	s_waitcnt lgkmcnt(2)
	v_cvt_pk_bf16_f32 v46, v56, v58
	s_waitcnt lgkmcnt(0)
	v_cvt_pk_bf16_f32 v47, v60, v62
	global_store_dwordx4 v[66:67], v[44:47], off nt
	s_andn2_b64 vcc, exec, s[10:11]
	s_mov_b32 s25, s15
	v_cvt_pk_bf16_f32 v44, v49, v51
	v_lshl_add_u64 v[48:49], v[64:65], 0, v[30:31]
	s_mov_b64 s[12:13], s[8:9]
	v_cvt_pk_bf16_f32 v45, v53, v55
	v_cvt_pk_bf16_f32 v46, v57, v59
	v_cvt_pk_bf16_f32 v47, v61, v63
	global_store_dwordx4 v[48:49], v[44:47], off nt
	s_barrier
	s_cbranch_vccz .LBB0_154

; __device__ __forceinline__ unsigned pk2(float lo, float hi) { unsigned r; asm("v_cvt_pk_bf16_f32 %0, %1, %2" : "=v"(r) : "v"(lo), "v"(hi)); return r; }
;     __device__ __forceinline__ const float* inp(int k) const { return (const float*)in[k]; }
; template <int TN, class DstFn>
; __device__ __forceinline__ void convert_T(const Ctx& c, const float* src, int nmat, int K, int N, DstFn dstfn) {
;     ...
;     for (long tix = c.bid; tix < ntiles; tix += c.G) {
;         const int m = (int)(tix / (tk * tn)); const int rem = (int)(tix % (tk * tn)); const int kt = rem / tn, nt = rem % tn;
; #pragma unroll
;         for (int i = 0; i < NI; ++i) { const int k = c.tid / TPR + KPI * i, n4 = (c.tid % TPR) * 4;
;             tile[k * LDT + n4 + 0] = v[i][0]; tile[k * LDT + n4 + 1] = v[i][1]; tile[k * LDT + n4 + 2] = v[i][2]; tile[k * LDT + n4 + 3] = v[i][3]; }
;         if (tix + c.G < ntiles) issue(tix + c.G);
;         __syncthreads();
;         { const int ch = c.tid & 7, nb = c.tid >> 3;
; #pragma unroll
;           for (int j = 0; j < TN / 64; ++j) { const int n = nb + 64 * j;
;               bf16_t* d = dstfn(m, nt * TN + n) + kt * 64 + ch * 8; u32x4 w;
; #pragma unroll
;               for (int e = 0; e < 4; ++e) w[e] = pk2(tile[(ch * 8 + 2 * e) * LDT + n], tile[(ch * 8 + 2 * e + 1) * LDT + n]);
;               *(u32x4*)d = w; } }
; __device__ __forceinline__ void phase_convert(const Ctx& c) {
;     ...
;       convert_T<256>(c, c.inp(23), 4 * NE, D, ED, [=](int m, int n) { return d + (size_t)((m >> 7) * NE1 + (m & 127)) * 512 * D + (size_t)((n >> 7) * 256 + (n & 127)) * D; });
.LBB0_156:
	s_ashr_i32 s34, s27, 31
	s_lshr_b32 s34, s34, 28
	s_add_u32 s26, s26, s34
	s_addc_u32 s27, s27, 0
	s_lshr_b64 s[26:27], s[26:27], 4
	s_ashr_i32 s27, s26, 7
	s_mulk_i32 s27, 0x81
	s_and_b32 s34, s26, 0x7f
	s_add_i32 s34, s27, s34
	s_ashr_i32 s35, s34, 31
	s_lshl_b64 s[34:35], s[34:35], 20
	s_add_u32 s34, s19, s34
	s_addc_u32 s35, s36, s35
	s_lshl_b32 s26, s26, 10
	s_sub_i32 s26, s39, s26
	s_ashr_i32 s27, s26, 31
	v_add_u32_e32 v57, 4, v33
	v_add_u32_e32 v59, 8, v33
	v_add_u32_e32 v61, 12, v33
	s_waitcnt lgkmcnt(0)
	s_barrier
	s_lshl_b64 s[26:27], s[26:27], 1
	ds_read2st64_b32 v[88:89], v33 offset1:1
	ds_read2st64_b32 v[90:91], v57 offset0:4 offset1:5
	ds_read2st64_b32 v[92:93], v59 offset0:8 offset1:9
	ds_read2st64_b32 v[94:95], v61 offset0:12 offset1:13
	ds_read2st64_b32 v[96:97], v33 offset0:2 offset1:3
	ds_read2st64_b32 v[98:99], v57 offset0:6 offset1:7
	ds_read2st64_b32 v[100:101], v59 offset0:10 offset1:11
	ds_read2st64_b32 v[102:103], v61 offset0:14 offset1:15
	v_add_u32_e32 v57, 16, v33
	v_add_u32_e32 v59, 20, v33
	v_add_u32_e32 v61, 24, v33
	v_add_u32_e32 v63, 28, v33
	s_add_u32 s26, s34, s26
	ds_read2st64_b32 v[104:105], v57 offset0:16 offset1:17
	ds_read2st64_b32 v[106:107], v59 offset0:20 offset1:21
	ds_read2st64_b32 v[108:109], v61 offset0:24 offset1:25
	ds_read2st64_b32 v[110:111], v63 offset0:28 offset1:29
	ds_read2st64_b32 v[112:113], v57 offset0:18 offset1:19
	ds_read2st64_b32 v[114:115], v59 offset0:22 offset1:23
	ds_read2st64_b32 v[116:117], v61 offset0:26 offset1:27
	ds_read2st64_b32 v[118:119], v63 offset0:30 offset1:31
	s_addc_u32 s27, s35, s27
	v_lshl_add_u64 v[86:87], s[26:27], 0, v[54:55]
	s_waitcnt lgkmcnt(14)
	v_cvt_pk_bf16_f32 v82, v88, v90
	s_waitcnt lgkmcnt(12)
	v_cvt_pk_bf16_f32 v83, v92, v94
	s_waitcnt lgkmcnt(6)
	v_cvt_pk_bf16_f32 v84, v104, v106
	s_waitcnt lgkmcnt(4)
	v_cvt_pk_bf16_f32 v85, v108, v110
	v_lshl_add_u64 v[120:121], v[86:87], 0, v[64:65]
	global_store_dwordx4 v[120:121], v[82:85], off nt
	s_andn2_b64 vcc, exec, s[2:3]
	s_mov_b32 s39, s23
	v_cvt_pk_bf16_f32 v82, v89, v91
	v_cvt_pk_bf16_f32 v83, v93, v95
	v_cvt_pk_bf16_f32 v84, v105, v107
	v_cvt_pk_bf16_f32 v85, v109, v111
	v_lshl_add_u64 v[88:89], v[86:87], 0, v[66:67]
	global_store_dwordx4 v[88:89], v[82:85], off nt
	v_lshl_add_u64 v[88:89], v[86:87], 0, v[68:69]
	v_lshl_add_u64 v[86:87], v[86:87], 0, v[70:71]
	v_cvt_pk_bf16_f32 v82, v96, v98
	v_cvt_pk_bf16_f32 v83, v100, v102
	s_waitcnt lgkmcnt(2)
	v_cvt_pk_bf16_f32 v84, v112, v114
	s_waitcnt lgkmcnt(0)
	v_cvt_pk_bf16_f32 v85, v116, v118
	s_mov_b64 s[26:27], s[24:25]
	global_store_dwordx4 v[88:89], v[82:85], off nt
	s_nop 1
	v_cvt_pk_bf16_f32 v82, v97, v99
	v_cvt_pk_bf16_f32 v83, v101, v103
	v_cvt_pk_bf16_f32 v84, v113, v115
	v_cvt_pk_bf16_f32 v85, v117, v119
	global_store_dwordx4 v[86:87], v[82:85], off nt
	s_barrier
	s_cbranch_vccz .LBB0_161

; __device__ __forceinline__ unsigned pk2(float lo, float hi) { unsigned r; asm("v_cvt_pk_bf16_f32 %0, %1, %2" : "=v"(r) : "v"(lo), "v"(hi)); return r; }
;     __device__ __forceinline__ const float* inp(int k) const { return (const float*)in[k]; }
; template <int TN, class DstFn>
; __device__ __forceinline__ void convert_T(const Ctx& c, const float* src, int nmat, int K, int N, DstFn dstfn) {
;     ...
;     for (long tix = c.bid; tix < ntiles; tix += c.G) {
;         const int m = (int)(tix / (tk * tn)); const int rem = (int)(tix % (tk * tn)); const int kt = rem / tn, nt = rem % tn;
; #pragma unroll
;         for (int i = 0; i < NI; ++i) { const int k = c.tid / TPR + KPI * i, n4 = (c.tid % TPR) * 4;
;             tile[k * LDT + n4 + 0] = v[i][0]; tile[k * LDT + n4 + 1] = v[i][1]; tile[k * LDT + n4 + 2] = v[i][2]; tile[k * LDT + n4 + 3] = v[i][3]; }
;         if (tix + c.G < ntiles) issue(tix + c.G);
;         __syncthreads();
;         { const int ch = c.tid & 7, nb = c.tid >> 3;
; #pragma unroll
;           for (int j = 0; j < TN / 64; ++j) { const int n = nb + 64 * j;
;               bf16_t* d = dstfn(m, nt * TN + n) + kt * 64 + ch * 8; u32x4 w;
; #pragma unroll
;               for (int e = 0; e < 4; ++e) w[e] = pk2(tile[(ch * 8 + 2 * e) * LDT + n], tile[(ch * 8 + 2 * e + 1) * LDT + n]);
;               *(u32x4*)d = w; } }
; __device__ __forceinline__ void phase_convert(const Ctx& c) {
;     ...
;       convert_T<256>(c, c.inp(24), 4 * NE, D, ED, [=](int m, int n) { return d + (size_t)((m >> 7) * NE1 + (m & 127)) * 512 * D + (size_t)((n >> 7) * 256 + 128 + (n & 127)) * D; });
.LBB0_162:
	s_ashr_i32 s22, s9, 31
	s_lshr_b32 s22, s22, 28
	s_add_u32 s8, s8, s22
	s_addc_u32 s9, s9, 0
	s_lshr_b64 s[8:9], s[8:9], 4
	s_ashr_i32 s9, s8, 7
	s_mulk_i32 s9, 0x81
	s_and_b32 s22, s8, 0x7f
	s_add_i32 s22, s9, s22
	s_ashr_i32 s23, s22, 31
	s_lshl_b64 s[22:23], s[22:23], 20
	s_add_u32 s22, s19, s22
	s_addc_u32 s23, s36, s23
	s_lshl_b32 s8, s8, 10
	s_sub_i32 s8, s38, s8
	s_waitcnt lgkmcnt(0)
	s_barrier
	s_ashr_i32 s9, s8, 31
	ds_read2st64_b32 v[74:75], v33 offset1:1
	v_add_u32_e32 v68, 4, v33
	v_add_u32_e32 v69, 8, v33
	v_add_u32_e32 v70, 12, v33
	s_lshl_b64 s[8:9], s[8:9], 1
	ds_read2st64_b32 v[82:83], v68 offset0:4 offset1:5
	ds_read2st64_b32 v[84:85], v69 offset0:8 offset1:9
	ds_read2st64_b32 v[86:87], v70 offset0:12 offset1:13
	ds_read2st64_b32 v[88:89], v33 offset0:2 offset1:3
	ds_read2st64_b32 v[90:91], v68 offset0:6 offset1:7
	s_waitcnt lgkmcnt(4)
	v_cvt_pk_bf16_f32 v68, v74, v82
	ds_read2st64_b32 v[92:93], v69 offset0:10 offset1:11
	ds_read2st64_b32 v[94:95], v70 offset0:14 offset1:15
	v_add_u32_e32 v70, 16, v33
	v_add_u32_e32 v71, 20, v33
	v_add_u32_e32 v74, 24, v33
	v_add_u32_e32 v81, 28, v33
	s_add_u32 s8, s22, s8
	ds_read2st64_b32 v[96:97], v70 offset0:16 offset1:17
	ds_read2st64_b32 v[98:99], v71 offset0:20 offset1:21
	ds_read2st64_b32 v[100:101], v74 offset0:24 offset1:25
	ds_read2st64_b32 v[102:103], v81 offset0:28 offset1:29
	ds_read2st64_b32 v[104:105], v70 offset0:18 offset1:19
	ds_read2st64_b32 v[106:107], v71 offset0:22 offset1:23
	ds_read2st64_b32 v[108:109], v74 offset0:26 offset1:27
	ds_read2st64_b32 v[110:111], v81 offset0:30 offset1:31
	s_addc_u32 s9, s23, s9
	v_lshl_add_u64 v[72:73], s[8:9], 0, v[54:55]
	s_waitcnt lgkmcnt(12)
	v_cvt_pk_bf16_f32 v69, v84, v86
	s_waitcnt lgkmcnt(6)
	v_cvt_pk_bf16_f32 v70, v96, v98
	s_waitcnt lgkmcnt(4)
	v_cvt_pk_bf16_f32 v71, v100, v102
	v_lshl_add_u64 v[112:113], v[72:73], 0, v[56:57]
	global_store_dwordx4 v[112:113], v[68:71], off nt
	s_andn2_b64 vcc, exec, s[2:3]
	s_mov_b32 s38, s13
	v_cvt_pk_bf16_f32 v68, v75, v83
	v_cvt_pk_bf16_f32 v69, v85, v87
	v_cvt_pk_bf16_f32 v70, v97, v99
	v_cvt_pk_bf16_f32 v71, v101, v103
	v_lshl_add_u64 v[74:75], v[72:73], 0, v[58:59]
	global_store_dwordx4 v[74:75], v[68:71], off nt
	v_lshl_add_u64 v[74:75], v[72:73], 0, v[60:61]
	v_lshl_add_u64 v[72:73], v[72:73], 0, v[62:63]
	v_cvt_pk_bf16_f32 v68, v88, v90
	v_cvt_pk_bf16_f32 v69, v92, v94
	s_waitcnt lgkmcnt(2)
	v_cvt_pk_bf16_f32 v70, v104, v106
	s_waitcnt lgkmcnt(0)
	v_cvt_pk_bf16_f32 v71, v108, v110
	s_mov_b64 s[8:9], s[20:21]
	global_store_dwordx4 v[74:75], v[68:71], off nt
	s_nop 1
	v_cvt_pk_bf16_f32 v68, v89, v91
	v_cvt_pk_bf16_f32 v69, v93, v95
	v_cvt_pk_bf16_f32 v70, v105, v107
	v_cvt_pk_bf16_f32 v71, v109, v111
	global_store_dwordx4 v[72:73], v[68:71], off nt
	s_barrier
	s_cbranch_vccz .LBB0_167

; __device__ __forceinline__ unsigned pk2(float lo, float hi) { unsigned r; asm("v_cvt_pk_bf16_f32 %0, %1, %2" : "=v"(r) : "v"(lo), "v"(hi)); return r; }
;     __device__ __forceinline__ const float* inp(int k) const { return (const float*)in[k]; }
; template <int TN, class DstFn>
; __device__ __forceinline__ void convert_T(const Ctx& c, const float* src, int nmat, int K, int N, DstFn dstfn) {
;     ...
;     for (long tix = c.bid; tix < ntiles; tix += c.G) {
;         const int m = (int)(tix / (tk * tn)); const int rem = (int)(tix % (tk * tn)); const int kt = rem / tn, nt = rem % tn;
; #pragma unroll
;         for (int i = 0; i < NI; ++i) { const int k = c.tid / TPR + KPI * i, n4 = (c.tid % TPR) * 4;
;             tile[k * LDT + n4 + 0] = v[i][0]; tile[k * LDT + n4 + 1] = v[i][1]; tile[k * LDT + n4 + 2] = v[i][2]; tile[k * LDT + n4 + 3] = v[i][3]; }
;         if (tix + c.G < ntiles) issue(tix + c.G);
;         __syncthreads();
;         { const int ch = c.tid & 7, nb = c.tid >> 3;
; #pragma unroll
;           for (int j = 0; j < TN / 64; ++j) { const int n = nb + 64 * j;
;               bf16_t* d = dstfn(m, nt * TN + n) + kt * 64 + ch * 8; u32x4 w;
; #pragma unroll
;               for (int e = 0; e < 4; ++e) w[e] = pk2(tile[(ch * 8 + 2 * e) * LDT + n], tile[(ch * 8 + 2 * e + 1) * LDT + n]);
;               *(u32x4*)d = w; } }
; __device__ __forceinline__ void phase_convert(const Ctx& c) {
;     ...
;       convert_T<256>(c, c.inp(26), 4, D, ED, [=](int m, int n) { return d + (size_t)(m * NE1 + NE) * 512 * D + (size_t)((n >> 7) * 256 + (n & 127)) * D; });
.LBB0_169:
	s_ashr_i32 s21, s27, 31
	s_lshr_b32 s21, s21, 28
	s_add_u32 s26, s26, s21
	s_addc_u32 s27, s27, 0
	s_lshr_b64 s[26:27], s[26:27], 4
	s_mul_i32 s21, s26, 0x81
	s_addk_i32 s21, 0x80
	s_ashr_i64 s[34:35], s[20:21], 12
	s_add_u32 s21, s19, s34
	s_addc_u32 s34, s36, s35
	s_lshl_b32 s26, s26, 10
	s_sub_i32 s26, s40, s26
	s_ashr_i32 s27, s26, 31
	v_add_u32_e32 v57, 4, v33
	v_add_u32_e32 v59, 8, v33
	v_add_u32_e32 v61, 12, v33
	s_waitcnt lgkmcnt(0)
	s_barrier
	s_lshl_b64 s[26:27], s[26:27], 1
	ds_read2st64_b32 v[84:85], v33 offset1:1
	ds_read2st64_b32 v[86:87], v57 offset0:4 offset1:5
	ds_read2st64_b32 v[88:89], v59 offset0:8 offset1:9
	ds_read2st64_b32 v[90:91], v61 offset0:12 offset1:13
	ds_read2st64_b32 v[92:93], v33 offset0:2 offset1:3
	ds_read2st64_b32 v[94:95], v57 offset0:6 offset1:7
	ds_read2st64_b32 v[96:97], v59 offset0:10 offset1:11
	ds_read2st64_b32 v[98:99], v61 offset0:14 offset1:15
	v_add_u32_e32 v57, 16, v33
	v_add_u32_e32 v59, 20, v33
	v_add_u32_e32 v61, 24, v33
	v_add_u32_e32 v63, 28, v33
	s_add_u32 s26, s21, s26
	ds_read2st64_b32 v[100:101], v57 offset0:16 offset1:17
	ds_read2st64_b32 v[102:103], v59 offset0:20 offset1:21
	ds_read2st64_b32 v[104:105], v61 offset0:24 offset1:25
	ds_read2st64_b32 v[106:107], v63 offset0:28 offset1:29
	ds_read2st64_b32 v[108:109], v57 offset0:18 offset1:19
	ds_read2st64_b32 v[110:111], v59 offset0:22 offset1:23
	ds_read2st64_b32 v[112:113], v61 offset0:26 offset1:27
	ds_read2st64_b32 v[114:115], v63 offset0:30 offset1:31
	s_addc_u32 s27, s34, s27
	v_lshl_add_u64 v[74:75], s[26:27], 0, v[54:55]
	s_waitcnt lgkmcnt(14)
	v_cvt_pk_bf16_f32 v80, v84, v86
	s_waitcnt lgkmcnt(12)
	v_cvt_pk_bf16_f32 v81, v88, v90
	s_waitcnt lgkmcnt(6)
	v_cvt_pk_bf16_f32 v82, v100, v102
	s_waitcnt lgkmcnt(4)
	v_cvt_pk_bf16_f32 v83, v104, v106
	v_lshl_add_u64 v[116:117], v[74:75], 0, v[64:65]
	global_store_dwordx4 v[116:117], v[80:83], off nt
	s_andn2_b64 vcc, exec, s[24:25]
	s_mov_b32 s40, s39
	v_cvt_pk_bf16_f32 v80, v85, v87
	v_cvt_pk_bf16_f32 v81, v89, v91
	v_cvt_pk_bf16_f32 v82, v101, v103
	v_cvt_pk_bf16_f32 v83, v105, v107
	v_lshl_add_u64 v[84:85], v[74:75], 0, v[66:67]
	global_store_dwordx4 v[84:85], v[80:83], off nt
	v_lshl_add_u64 v[84:85], v[74:75], 0, v[68:69]
	v_lshl_add_u64 v[74:75], v[74:75], 0, v[70:71]
	v_cvt_pk_bf16_f32 v80, v92, v94
	v_cvt_pk_bf16_f32 v81, v96, v98
	s_waitcnt lgkmcnt(2)
	v_cvt_pk_bf16_f32 v82, v108, v110
	s_waitcnt lgkmcnt(0)
	v_cvt_pk_bf16_f32 v83, v112, v114
	s_mov_b64 s[26:27], s[22:23]
	global_store_dwordx4 v[84:85], v[80:83], off nt
	s_nop 1
	v_cvt_pk_bf16_f32 v80, v93, v95
	v_cvt_pk_bf16_f32 v81, v97, v99
	v_cvt_pk_bf16_f32 v82, v109, v111
	v_cvt_pk_bf16_f32 v83, v113, v115
	global_store_dwordx4 v[74:75], v[80:83], off nt
	s_barrier
	s_cbranch_vccz .LBB0_174

; __device__ __forceinline__ unsigned pk2(float lo, float hi) { unsigned r; asm("v_cvt_pk_bf16_f32 %0, %1, %2" : "=v"(r) : "v"(lo), "v"(hi)); return r; }
;     __device__ __forceinline__ const float* inp(int k) const { return (const float*)in[k]; }
; template <int TN, class DstFn>
; __device__ __forceinline__ void convert_T(const Ctx& c, const float* src, int nmat, int K, int N, DstFn dstfn) {
;     ...
;     for (long tix = c.bid; tix < ntiles; tix += c.G) {
;         const int m = (int)(tix / (tk * tn)); const int rem = (int)(tix % (tk * tn)); const int kt = rem / tn, nt = rem % tn;
; #pragma unroll
;         for (int i = 0; i < NI; ++i) { const int k = c.tid / TPR + KPI * i, n4 = (c.tid % TPR) * 4;
;             tile[k * LDT + n4 + 0] = v[i][0]; tile[k * LDT + n4 + 1] = v[i][1]; tile[k * LDT + n4 + 2] = v[i][2]; tile[k * LDT + n4 + 3] = v[i][3]; }
;         if (tix + c.G < ntiles) issue(tix + c.G);
;         __syncthreads();
;         { const int ch = c.tid & 7, nb = c.tid >> 3;
; #pragma unroll
;           for (int j = 0; j < TN / 64; ++j) { const int n = nb + 64 * j;
;               bf16_t* d = dstfn(m, nt * TN + n) + kt * 64 + ch * 8; u32x4 w;
; #pragma unroll
;               for (int e = 0; e < 4; ++e) w[e] = pk2(tile[(ch * 8 + 2 * e) * LDT + n], tile[(ch * 8 + 2 * e + 1) * LDT + n]);
;               *(u32x4*)d = w; } }
; __device__ __forceinline__ void phase_convert(const Ctx& c) {
;     ...
;       convert_T<256>(c, c.inp(27), 4, D, ED, [=](int m, int n) { return d + (size_t)(m * NE1 + NE) * 512 * D + (size_t)((n >> 7) * 256 + 128 + (n & 127)) * D; }); }
.LBB0_175:
	s_ashr_i32 s11, s7, 31
	s_lshr_b32 s11, s11, 28
	s_add_u32 s6, s6, s11
	s_addc_u32 s7, s7, 0
	s_lshr_b64 s[6:7], s[6:7], 4
	s_mul_i32 s7, s6, 0x81
	s_add_i32 s11, s7, 0x80
	s_ashr_i64 s[22:23], s[10:11], 12
	s_add_u32 s11, s19, s22
	s_addc_u32 s22, s36, s23
	s_lshl_b32 s6, s6, 10
	s_sub_i32 s6, s38, s6
	s_waitcnt lgkmcnt(0)
	s_barrier
	s_ashr_i32 s7, s6, 31
	ds_read2st64_b32 v[70:71], v33 offset1:1
	v_add_u32_e32 v64, 4, v33
	v_add_u32_e32 v65, 8, v33
	v_add_u32_e32 v66, 12, v33
	s_lshl_b64 s[6:7], s[6:7], 1
	ds_read2st64_b32 v[74:75], v64 offset0:4 offset1:5
	ds_read2st64_b32 v[80:81], v65 offset0:8 offset1:9
	ds_read2st64_b32 v[82:83], v66 offset0:12 offset1:13
	ds_read2st64_b32 v[84:85], v33 offset0:2 offset1:3
	ds_read2st64_b32 v[86:87], v64 offset0:6 offset1:7
	s_waitcnt lgkmcnt(4)
	v_cvt_pk_bf16_f32 v64, v70, v74
	ds_read2st64_b32 v[88:89], v65 offset0:10 offset1:11
	ds_read2st64_b32 v[90:91], v66 offset0:14 offset1:15
	v_add_u32_e32 v66, 16, v33
	v_add_u32_e32 v67, 20, v33
	v_add_u32_e32 v70, 24, v33
	v_add_u32_e32 v73, 28, v33
	s_add_u32 s6, s11, s6
	ds_read2st64_b32 v[92:93], v66 offset0:16 offset1:17
	ds_read2st64_b32 v[94:95], v67 offset0:20 offset1:21
	ds_read2st64_b32 v[96:97], v70 offset0:24 offset1:25
	ds_read2st64_b32 v[98:99], v73 offset0:28 offset1:29
	ds_read2st64_b32 v[100:101], v66 offset0:18 offset1:19
	ds_read2st64_b32 v[102:103], v67 offset0:22 offset1:23
	ds_read2st64_b32 v[104:105], v70 offset0:26 offset1:27
	ds_read2st64_b32 v[106:107], v73 offset0:30 offset1:31
	s_addc_u32 s7, s22, s7
	v_lshl_add_u64 v[68:69], s[6:7], 0, v[54:55]
	s_waitcnt lgkmcnt(12)
	v_cvt_pk_bf16_f32 v65, v80, v82
	s_waitcnt lgkmcnt(6)
	v_cvt_pk_bf16_f32 v66, v92, v94
	s_waitcnt lgkmcnt(4)
	v_cvt_pk_bf16_f32 v67, v96, v98
	v_lshl_add_u64 v[108:109], v[68:69], 0, v[56:57]
	global_store_dwordx4 v[108:109], v[64:67], off nt
	s_andn2_b64 vcc, exec, s[20:21]
	s_mov_b32 s38, s24
	v_cvt_pk_bf16_f32 v64, v71, v75
	v_cvt_pk_bf16_f32 v65, v81, v83
	v_cvt_pk_bf16_f32 v66, v93, v95
	v_cvt_pk_bf16_f32 v67, v97, v99
	v_lshl_add_u64 v[70:71], v[68:69], 0, v[58:59]
	global_store_dwordx4 v[70:71], v[64:67], off nt
	v_lshl_add_u64 v[70:71], v[68:69], 0, v[60:61]
	v_lshl_add_u64 v[68:69], v[68:69], 0, v[62:63]
	v_cvt_pk_bf16_f32 v64, v84, v86
	v_cvt_pk_bf16_f32 v65, v88, v90
	s_waitcnt lgkmcnt(2)
	v_cvt_pk_bf16_f32 v66, v100, v102
	s_waitcnt lgkmcnt(0)
	v_cvt_pk_bf16_f32 v67, v104, v106
	s_mov_b64 s[6:7], s[12:13]
	global_store_dwordx4 v[70:71], v[64:67], off nt
	s_nop 1
	v_cvt_pk_bf16_f32 v64, v85, v87
	v_cvt_pk_bf16_f32 v65, v89, v91
	v_cvt_pk_bf16_f32 v66, v101, v103
	v_cvt_pk_bf16_f32 v67, v105, v107
	global_store_dwordx4 v[68:69], v[64:67], off nt
	s_barrier
	s_cbranch_vccz .LBB0_180

; __device__ __forceinline__ unsigned pk2(float lo, float hi) { unsigned r; asm("v_cvt_pk_bf16_f32 %0, %1, %2" : "=v"(r) : "v"(lo), "v"(hi)); return r; }
;     __device__ __forceinline__ const float* inp(int k) const { return (const float*)in[k]; }
; template <int TN, class DstFn>
; __device__ __forceinline__ void convert_T(const Ctx& c, const float* src, int nmat, int K, int N, DstFn dstfn) {
;     ...
;     for (long tix = c.bid; tix < ntiles; tix += c.G) {
;         const int m = (int)(tix / (tk * tn)); const int rem = (int)(tix % (tk * tn)); const int kt = rem / tn, nt = rem % tn;
; #pragma unroll
;         for (int i = 0; i < NI; ++i) { const int k = c.tid / TPR + KPI * i, n4 = (c.tid % TPR) * 4;
;             tile[k * LDT + n4 + 0] = v[i][0]; tile[k * LDT + n4 + 1] = v[i][1]; tile[k * LDT + n4 + 2] = v[i][2]; tile[k * LDT + n4 + 3] = v[i][3]; }
;         if (tix + c.G < ntiles) issue(tix + c.G);
;         __syncthreads();
;         { const int ch = c.tid & 7, nb = c.tid >> 3;
; #pragma unroll
;           for (int j = 0; j < TN / 64; ++j) { const int n = nb + 64 * j;
;               bf16_t* d = dstfn(m, nt * TN + n) + kt * 64 + ch * 8; u32x4 w;
; #pragma unroll
;               for (int e = 0; e < 4; ++e) w[e] = pk2(tile[(ch * 8 + 2 * e) * LDT + n], tile[(ch * 8 + 2 * e + 1) * LDT + n]);
;               *(u32x4*)d = w; } }
; __device__ __forceinline__ void phase_convert(const Ctx& c) {
;     ...
;       convert_T<256>(c, c.inp(12), 10, 256, 256, [=](int m, int n) { return d + (size_t)(m * 2 + 0) * 65536 + (size_t)n * 256; });
.LBB0_182:
	s_ashr_i32 s34, s27, 31
	s_lshr_b32 s34, s34, 30
	s_add_u32 s26, s26, s34
	s_addc_u32 s27, s27, 0
	s_lshr_b64 s[26:27], s[26:27], 2
	s_lshl_b32 s34, s26, 1
	s_ashr_i32 s35, s34, 31
	s_lshl_b64 s[34:35], s[34:35], 17
	s_add_u32 s34, s19, s34
	s_addc_u32 s35, s36, s35
	s_lshl_b32 s26, s26, 8
	s_sub_i32 s26, s39, s26
	s_waitcnt lgkmcnt(0)
	s_barrier
	s_ashr_i32 s27, s26, 31
	ds_read2st64_b32 v[72:73], v33 offset1:1
	v_add_u32_e32 v65, 4, v33
	v_add_u32_e32 v67, 8, v33
	v_add_u32_e32 v68, 12, v33
	s_lshl_b64 s[26:27], s[26:27], 1
	ds_read2st64_b32 v[74:75], v65 offset0:4 offset1:5
	ds_read2st64_b32 v[80:81], v67 offset0:8 offset1:9
	ds_read2st64_b32 v[82:83], v68 offset0:12 offset1:13
	ds_read2st64_b32 v[84:85], v33 offset0:2 offset1:3
	ds_read2st64_b32 v[86:87], v65 offset0:6 offset1:7
	s_waitcnt lgkmcnt(4)
	v_cvt_pk_bf16_f32 v66, v72, v74
	ds_read2st64_b32 v[88:89], v67 offset0:10 offset1:11
	ds_read2st64_b32 v[90:91], v68 offset0:14 offset1:15
	v_add_u32_e32 v65, 16, v33
	v_add_u32_e32 v68, 20, v33
	v_add_u32_e32 v69, 24, v33
	v_add_u32_e32 v72, 28, v33
	s_add_u32 s26, s34, s26
	ds_read2st64_b32 v[92:93], v65 offset0:16 offset1:17
	ds_read2st64_b32 v[94:95], v68 offset0:20 offset1:21
	ds_read2st64_b32 v[96:97], v69 offset0:24 offset1:25
	ds_read2st64_b32 v[98:99], v72 offset0:28 offset1:29
	ds_read2st64_b32 v[100:101], v65 offset0:18 offset1:19
	ds_read2st64_b32 v[102:103], v68 offset0:22 offset1:23
	ds_read2st64_b32 v[104:105], v69 offset0:26 offset1:27
	ds_read2st64_b32 v[106:107], v72 offset0:30 offset1:31
	s_addc_u32 s27, s35, s27
	v_lshl_add_u64 v[70:71], s[26:27], 0, v[54:55]
	s_waitcnt lgkmcnt(12)
	v_cvt_pk_bf16_f32 v67, v80, v82
	s_waitcnt lgkmcnt(6)
	v_cvt_pk_bf16_f32 v68, v92, v94
	s_waitcnt lgkmcnt(4)
	v_cvt_pk_bf16_f32 v69, v96, v98
	v_lshl_add_u64 v[108:109], v[70:71], 0, v[56:57]
	global_store_dwordx4 v[108:109], v[66:69], off nt
	s_andn2_b64 vcc, exec, s[24:25]
	s_mov_b32 s39, s21
	v_cvt_pk_bf16_f32 v66, v73, v75
	v_cvt_pk_bf16_f32 v67, v81, v83
	v_cvt_pk_bf16_f32 v68, v93, v95
	v_cvt_pk_bf16_f32 v69, v97, v99
	v_lshl_add_u64 v[72:73], v[70:71], 0, v[58:59]
	global_store_dwordx4 v[72:73], v[66:69], off nt
	v_lshl_add_u64 v[72:73], v[70:71], 0, v[60:61]
	v_lshl_add_u64 v[70:71], v[70:71], 0, v[62:63]
	v_cvt_pk_bf16_f32 v66, v84, v86
	v_cvt_pk_bf16_f32 v67, v88, v90
	s_waitcnt lgkmcnt(2)
	v_cvt_pk_bf16_f32 v68, v100, v102
	s_waitcnt lgkmcnt(0)
	v_cvt_pk_bf16_f32 v69, v104, v106
	s_mov_b64 s[26:27], s[22:23]
	global_store_dwordx4 v[72:73], v[66:69], off nt
	s_nop 1
	v_cvt_pk_bf16_f32 v66, v85, v87
	v_cvt_pk_bf16_f32 v67, v89, v91
	v_cvt_pk_bf16_f32 v68, v101, v103
	v_cvt_pk_bf16_f32 v69, v105, v107
	global_store_dwordx4 v[70:71], v[66:69], off nt
	s_barrier
	s_cbranch_vccz .LBB0_187

; __device__ __forceinline__ unsigned pk2(float lo, float hi) { unsigned r; asm("v_cvt_pk_bf16_f32 %0, %1, %2" : "=v"(r) : "v"(lo), "v"(hi)); return r; }
;     __device__ __forceinline__ const float* inp(int k) const { return (const float*)in[k]; }
; template <int TN, class DstFn>
; __device__ __forceinline__ void convert_T(const Ctx& c, const float* src, int nmat, int K, int N, DstFn dstfn) {
;     ...
;     for (long tix = c.bid; tix < ntiles; tix += c.G) {
;         const int m = (int)(tix / (tk * tn)); const int rem = (int)(tix % (tk * tn)); const int kt = rem / tn, nt = rem % tn;
; #pragma unroll
;         for (int i = 0; i < NI; ++i) { const int k = c.tid / TPR + KPI * i, n4 = (c.tid % TPR) * 4;
;             tile[k * LDT + n4 + 0] = v[i][0]; tile[k * LDT + n4 + 1] = v[i][1]; tile[k * LDT + n4 + 2] = v[i][2]; tile[k * LDT + n4 + 3] = v[i][3]; }
;         if (tix + c.G < ntiles) issue(tix + c.G);
;         __syncthreads();
;         { const int ch = c.tid & 7, nb = c.tid >> 3;
; #pragma unroll
;           for (int j = 0; j < TN / 64; ++j) { const int n = nb + 64 * j;
;               bf16_t* d = dstfn(m, nt * TN + n) + kt * 64 + ch * 8; u32x4 w;
; #pragma unroll
;               for (int e = 0; e < 4; ++e) w[e] = pk2(tile[(ch * 8 + 2 * e) * LDT + n], tile[(ch * 8 + 2 * e + 1) * LDT + n]);
;               *(u32x4*)d = w; } }
; __device__ __forceinline__ void phase_convert(const Ctx& c) {
;     ...
;       convert_T<256>(c, c.inp(14), 10, 256, 256, [=](int m, int n) { return d + (size_t)(m * 2 + 1) * 65536 + (size_t)n * 256; });
.LBB0_188:
	s_ashr_i32 s22, s7, 31
	s_lshr_b32 s22, s22, 30
	s_add_u32 s6, s6, s22
	s_addc_u32 s7, s7, 0
	s_lshr_b64 s[6:7], s[6:7], 2
	s_lshl_b32 s7, s6, 1
	s_or_b32 s22, s7, 1
	s_ashr_i32 s23, s22, 31
	s_lshl_b64 s[22:23], s[22:23], 17
	s_add_u32 s22, s19, s22
	s_addc_u32 s23, s36, s23
	s_lshl_b32 s6, s6, 8
	s_sub_i32 s6, s38, s6
	s_waitcnt lgkmcnt(0)
	s_barrier
	s_ashr_i32 s7, s6, 31
	ds_read2st64_b32 v[72:73], v33 offset1:1
	v_add_u32_e32 v65, 4, v33
	v_add_u32_e32 v67, 8, v33
	v_add_u32_e32 v68, 12, v33
	s_lshl_b64 s[6:7], s[6:7], 1
	ds_read2st64_b32 v[74:75], v65 offset0:4 offset1:5
	ds_read2st64_b32 v[80:81], v67 offset0:8 offset1:9
	ds_read2st64_b32 v[82:83], v68 offset0:12 offset1:13
	ds_read2st64_b32 v[84:85], v33 offset0:2 offset1:3
	ds_read2st64_b32 v[86:87], v65 offset0:6 offset1:7
	s_waitcnt lgkmcnt(4)
	v_cvt_pk_bf16_f32 v66, v72, v74
	ds_read2st64_b32 v[88:89], v67 offset0:10 offset1:11
	ds_read2st64_b32 v[90:91], v68 offset0:14 offset1:15
	v_add_u32_e32 v65, 16, v33
	v_add_u32_e32 v68, 20, v33
	v_add_u32_e32 v69, 24, v33
	v_add_u32_e32 v72, 28, v33
	s_add_u32 s6, s22, s6
	ds_read2st64_b32 v[92:93], v65 offset0:16 offset1:17
	ds_read2st64_b32 v[94:95], v68 offset0:20 offset1:21
	ds_read2st64_b32 v[96:97], v69 offset0:24 offset1:25
	ds_read2st64_b32 v[98:99], v72 offset0:28 offset1:29
	ds_read2st64_b32 v[100:101], v65 offset0:18 offset1:19
	ds_read2st64_b32 v[102:103], v68 offset0:22 offset1:23
	ds_read2st64_b32 v[104:105], v69 offset0:26 offset1:27
	ds_read2st64_b32 v[106:107], v72 offset0:30 offset1:31
	s_addc_u32 s7, s23, s7
	v_lshl_add_u64 v[70:71], s[6:7], 0, v[54:55]
	s_waitcnt lgkmcnt(12)
	v_cvt_pk_bf16_f32 v67, v80, v82
	s_waitcnt lgkmcnt(6)
	v_cvt_pk_bf16_f32 v68, v92, v94
	s_waitcnt lgkmcnt(4)
	v_cvt_pk_bf16_f32 v69, v96, v98
	v_lshl_add_u64 v[108:109], v[70:71], 0, v[56:57]
	global_store_dwordx4 v[108:109], v[66:69], off nt
	s_andn2_b64 vcc, exec, s[20:21]
	s_mov_b32 s38, s11
	v_cvt_pk_bf16_f32 v66, v73, v75
	v_cvt_pk_bf16_f32 v67, v81, v83
	v_cvt_pk_bf16_f32 v68, v93, v95
	v_cvt_pk_bf16_f32 v69, v97, v99
	v_lshl_add_u64 v[72:73], v[70:71], 0, v[58:59]
	global_store_dwordx4 v[72:73], v[66:69], off nt
	v_lshl_add_u64 v[72:73], v[70:71], 0, v[60:61]
	v_lshl_add_u64 v[70:71], v[70:71], 0, v[62:63]
	v_cvt_pk_bf16_f32 v66, v84, v86
	v_cvt_pk_bf16_f32 v67, v88, v90
	s_waitcnt lgkmcnt(2)
	v_cvt_pk_bf16_f32 v68, v100, v102
	s_waitcnt lgkmcnt(0)
	v_cvt_pk_bf16_f32 v69, v104, v106
	s_mov_b64 s[6:7], s[12:13]
	global_store_dwordx4 v[72:73], v[66:69], off nt
	s_nop 1
	v_cvt_pk_bf16_f32 v66, v85, v87
	v_cvt_pk_bf16_f32 v67, v89, v91
	v_cvt_pk_bf16_f32 v68, v101, v103
	v_cvt_pk_bf16_f32 v69, v105, v107
	global_store_dwordx4 v[70:71], v[66:69], off nt
	s_barrier
	s_cbranch_vccz .LBB0_193

; __device__ __forceinline__ unsigned pk2(float lo, float hi) { unsigned r; asm("v_cvt_pk_bf16_f32 %0, %1, %2" : "=v"(r) : "v"(lo), "v"(hi)); return r; }
;     __device__ __forceinline__ const float* inp(int k) const { return (const float*)in[k]; }
; template <int TN, class DstFn>
; __device__ __forceinline__ void convert_T(const Ctx& c, const float* src, int nmat, int K, int N, DstFn dstfn) {
;     ...
;     for (long tix = c.bid; tix < ntiles; tix += c.G) {
;         const int m = (int)(tix / (tk * tn)); const int rem = (int)(tix % (tk * tn)); const int kt = rem / tn, nt = rem % tn;
; #pragma unroll
;         for (int i = 0; i < NI; ++i) { const int k = c.tid / TPR + KPI * i, n4 = (c.tid % TPR) * 4;
;             tile[k * LDT + n4 + 0] = v[i][0]; tile[k * LDT + n4 + 1] = v[i][1]; tile[k * LDT + n4 + 2] = v[i][2]; tile[k * LDT + n4 + 3] = v[i][3]; }
;         if (tix + c.G < ntiles) issue(tix + c.G);
;         __syncthreads();
;         { const int ch = c.tid & 7, nb = c.tid >> 3;
; #pragma unroll
;           for (int j = 0; j < TN / 64; ++j) { const int n = nb + 64 * j;
;               bf16_t* d = dstfn(m, nt * TN + n) + kt * 64 + ch * 8; u32x4 w;
; #pragma unroll
;               for (int e = 0; e < 4; ++e) w[e] = pk2(tile[(ch * 8 + 2 * e) * LDT + n], tile[(ch * 8 + 2 * e + 1) * LDT + n]);
;               *(u32x4*)d = w; } }
; __device__ __forceinline__ void phase_convert(const Ctx& c) {
;     ...
;       convert_T<256>(c, c.inp(25), 4 * NE, ED, D, [=](int m, int n) { return d + (size_t)((m >> 7) * NE1 + (m & 127)) * D * ED + (size_t)n * ED; });
.LBB0_198:
	s_ashr_i32 s9, s13, 31
	s_lshr_b32 s9, s9, 28
	s_add_u32 s20, s12, s9
	s_addc_u32 s21, s13, 0
	s_lshr_b64 s[20:21], s[20:21], 4
	s_lshl_b32 s9, s20, 4
	s_sub_i32 s9, s12, s9
	s_bfe_i32 s12, s9, 0x80000
	s_bfe_u32 s12, s12, 0x2000d
	s_add_i32 s12, s9, s12
	s_bfe_i32 s13, s12, 0x80000
	s_and_b32 s12, s12, 0xfc
	s_sub_i32 s9, s9, s12
	s_ashr_i32 s12, s20, 7
	s_sext_i32_i16 s15, s13
	s_mulk_i32 s12, 0x81
	s_and_b32 s13, s20, 0x7f
	s_add_i32 s12, s12, s13
	s_ashr_i32 s13, s12, 31
	s_lshl_b64 s[12:13], s[12:13], 19
	s_add_u32 s19, s16, s12
	s_addc_u32 s20, s17, s13
	s_lshl_b32 s12, s15, 4
	s_sext_i32_i8 s9, s9
	s_andn2_b32 s12, s12, 63
	s_ashr_i32 s13, s12, 31
	v_lshl_add_u32 v64, s9, 8, v32
	s_lshl_b64 s[12:13], s[12:13], 1
	v_ashrrev_i32_e32 v65, 31, v64
	v_add_u32_e32 v57, 4, v33
	v_add_u32_e32 v59, 8, v33
	v_add_u32_e32 v60, 12, v33
	s_waitcnt lgkmcnt(0)
	s_barrier
	s_add_u32 s12, s19, s12
	v_lshlrev_b64 v[66:67], 9, v[64:65]
	ds_read2st64_b32 v[68:69], v33 offset1:1
	ds_read2st64_b32 v[70:71], v57 offset0:4 offset1:5
	ds_read2st64_b32 v[72:73], v59 offset0:8 offset1:9
	ds_read2st64_b32 v[74:75], v60 offset0:12 offset1:13
	ds_read2st64_b32 v[80:81], v33 offset0:2 offset1:3
	ds_read2st64_b32 v[82:83], v57 offset0:6 offset1:7
	ds_read2st64_b32 v[84:85], v59 offset0:10 offset1:11
	ds_read2st64_b32 v[86:87], v60 offset0:14 offset1:15
	v_add_u32_e32 v57, 16, v33
	v_add_u32_e32 v60, 20, v33
	v_add_u32_e32 v61, 24, v33
	v_add_u32_e32 v65, 28, v33
	s_addc_u32 s13, s20, s13
	ds_read2st64_b32 v[88:89], v57 offset0:16 offset1:17
	ds_read2st64_b32 v[90:91], v60 offset0:20 offset1:21
	ds_read2st64_b32 v[92:93], v61 offset0:24 offset1:25
	ds_read2st64_b32 v[94:95], v65 offset0:28 offset1:29
	ds_read2st64_b32 v[96:97], v57 offset0:18 offset1:19
	ds_read2st64_b32 v[98:99], v60 offset0:22 offset1:23
	v_lshl_add_u64 v[62:63], s[12:13], 0, v[52:53]
	s_waitcnt lgkmcnt(12)
	v_cvt_pk_bf16_f32 v58, v68, v70
	v_lshl_add_u64 v[66:67], v[62:63], 0, v[66:67]
	s_waitcnt lgkmcnt(10)
	v_cvt_pk_bf16_f32 v59, v72, v74
	s_waitcnt lgkmcnt(4)
	v_cvt_pk_bf16_f32 v60, v88, v90
	ds_read2st64_b32 v[100:101], v61 offset0:26 offset1:27
	ds_read2st64_b32 v[102:103], v65 offset0:30 offset1:31
	s_waitcnt lgkmcnt(4)
	v_cvt_pk_bf16_f32 v61, v92, v94
	global_store_dwordx4 v[66:67], v[58:61], off nt
	s_andn2_b64 vcc, exec, s[4:5]
	s_mov_b64 s[12:13], s[10:11]
	v_add_u32_e32 v58, 64, v64
	v_ashrrev_i32_e32 v59, 31, v58
	v_lshlrev_b64 v[66:67], 9, v[58:59]
	v_cvt_pk_bf16_f32 v58, v69, v71
	v_lshl_add_u64 v[66:67], v[62:63], 0, v[66:67]
	v_cvt_pk_bf16_f32 v59, v73, v75
	v_cvt_pk_bf16_f32 v60, v89, v91
	v_cvt_pk_bf16_f32 v61, v93, v95
	global_store_dwordx4 v[66:67], v[58:61], off nt
	s_nop 1
	v_add_u32_e32 v58, 0x80, v64
	v_ashrrev_i32_e32 v59, 31, v58
	v_lshlrev_b64 v[66:67], 9, v[58:59]
	v_cvt_pk_bf16_f32 v58, v80, v82
	v_lshl_add_u64 v[66:67], v[62:63], 0, v[66:67]
	v_cvt_pk_bf16_f32 v59, v84, v86
	s_waitcnt lgkmcnt(2)
	v_cvt_pk_bf16_f32 v60, v96, v98
	s_waitcnt lgkmcnt(0)
	v_cvt_pk_bf16_f32 v61, v100, v102
	global_store_dwordx4 v[66:67], v[58:61], off nt
	s_nop 1
	v_add_u32_e32 v58, 0xc0, v64
	v_ashrrev_i32_e32 v59, 31, v58
	v_lshlrev_b64 v[64:65], 9, v[58:59]
	v_lshl_add_u64 v[62:63], v[62:63], 0, v[64:65]
	v_cvt_pk_bf16_f32 v58, v81, v83
	v_cvt_pk_bf16_f32 v59, v85, v87
	v_cvt_pk_bf16_f32 v60, v97, v99
	v_cvt_pk_bf16_f32 v61, v101, v103
	global_store_dwordx4 v[62:63], v[58:61], off nt
	s_barrier
	s_cbranch_vccz .LBB0_201

; __device__ __forceinline__ unsigned pk2(float lo, float hi) { unsigned r; asm("v_cvt_pk_bf16_f32 %0, %1, %2" : "=v"(r) : "v"(lo), "v"(hi)); return r; }
;     __device__ __forceinline__ const float* inp(int k) const { return (const float*)in[k]; }
; template <int TN, class DstFn>
; __device__ __forceinline__ void convert_T(const Ctx& c, const float* src, int nmat, int K, int N, DstFn dstfn) {
;     ...
;     for (long tix = c.bid; tix < ntiles; tix += c.G) {
;         const int m = (int)(tix / (tk * tn)); const int rem = (int)(tix % (tk * tn)); const int kt = rem / tn, nt = rem % tn;
; #pragma unroll
;         for (int i = 0; i < NI; ++i) { const int k = c.tid / TPR + KPI * i, n4 = (c.tid % TPR) * 4;
;             tile[k * LDT + n4 + 0] = v[i][0]; tile[k * LDT + n4 + 1] = v[i][1]; tile[k * LDT + n4 + 2] = v[i][2]; tile[k * LDT + n4 + 3] = v[i][3]; }
;         if (tix + c.G < ntiles) issue(tix + c.G);
;         __syncthreads();
;         { const int ch = c.tid & 7, nb = c.tid >> 3;
; #pragma unroll
;           for (int j = 0; j < TN / 64; ++j) { const int n = nb + 64 * j;
;               bf16_t* d = dstfn(m, nt * TN + n) + kt * 64 + ch * 8; u32x4 w;
; #pragma unroll
;               for (int e = 0; e < 4; ++e) w[e] = pk2(tile[(ch * 8 + 2 * e) * LDT + n], tile[(ch * 8 + 2 * e + 1) * LDT + n]);
;               *(u32x4*)d = w; } }
; __device__ __forceinline__ void phase_convert(const Ctx& c) {
;     ...
;       convert_T<256>(c, c.inp(28), 4, ED, D, [=](int m, int n) { return d + (size_t)(m * NE1 + NE) * D * ED + (size_t)n * ED; }); }
.LBB0_203:
	s_ashr_i32 s5, s15, 31
	s_lshr_b32 s5, s5, 28
	s_add_u32 s12, s14, s5
	s_addc_u32 s13, s15, 0
	s_lshr_b64 s[12:13], s[12:13], 4
	s_lshl_b32 s5, s12, 4
	s_sub_i32 s5, s14, s5
	s_bfe_i32 s11, s5, 0x80000
	s_bfe_u32 s11, s11, 0x2000d
	s_add_i32 s11, s5, s11
	s_bfe_i32 s13, s11, 0x80000
	s_and_b32 s11, s11, 0xfc
	s_sub_i32 s5, s5, s11
	s_sext_i32_i8 s11, s5
	s_mul_i32 s5, s12, 0x81
	s_addk_i32 s5, 0x80
	s_sext_i32_i16 s14, s13
	s_ashr_i64 s[12:13], s[4:5], 13
	s_add_u32 s5, s16, s12
	s_addc_u32 s15, s17, s13
	s_lshl_b32 s12, s14, 4
	s_andn2_b32 s12, s12, 63
	s_ashr_i32 s13, s12, 31
	v_lshl_add_u32 v62, s11, 8, v32
	s_lshl_b64 s[12:13], s[12:13], 1
	v_ashrrev_i32_e32 v63, 31, v62
	v_add_u32_e32 v55, 4, v33
	v_add_u32_e32 v57, 8, v33
	v_add_u32_e32 v58, 12, v33
	s_waitcnt lgkmcnt(0)
	s_barrier
	s_add_u32 s12, s5, s12
	v_lshlrev_b64 v[64:65], 9, v[62:63]
	ds_read2st64_b32 v[66:67], v33 offset1:1
	ds_read2st64_b32 v[68:69], v55 offset0:4 offset1:5
	ds_read2st64_b32 v[70:71], v57 offset0:8 offset1:9
	ds_read2st64_b32 v[72:73], v58 offset0:12 offset1:13
	ds_read2st64_b32 v[74:75], v33 offset0:2 offset1:3
	ds_read2st64_b32 v[78:79], v55 offset0:6 offset1:7
	ds_read2st64_b32 v[80:81], v57 offset0:10 offset1:11
	ds_read2st64_b32 v[82:83], v58 offset0:14 offset1:15
	v_add_u32_e32 v55, 16, v33
	v_add_u32_e32 v58, 20, v33
	v_add_u32_e32 v59, 24, v33
	v_add_u32_e32 v63, 28, v33
	s_addc_u32 s13, s15, s13
	ds_read2st64_b32 v[84:85], v55 offset0:16 offset1:17
	ds_read2st64_b32 v[86:87], v58 offset0:20 offset1:21
	ds_read2st64_b32 v[88:89], v59 offset0:24 offset1:25
	ds_read2st64_b32 v[90:91], v63 offset0:28 offset1:29
	ds_read2st64_b32 v[92:93], v55 offset0:18 offset1:19
	ds_read2st64_b32 v[94:95], v58 offset0:22 offset1:23
	v_lshl_add_u64 v[60:61], s[12:13], 0, v[52:53]
	s_waitcnt lgkmcnt(12)
	v_cvt_pk_bf16_f32 v56, v66, v68
	v_lshl_add_u64 v[64:65], v[60:61], 0, v[64:65]
	s_waitcnt lgkmcnt(10)
	v_cvt_pk_bf16_f32 v57, v70, v72
	s_waitcnt lgkmcnt(4)
	v_cvt_pk_bf16_f32 v58, v84, v86
	ds_read2st64_b32 v[96:97], v59 offset0:26 offset1:27
	ds_read2st64_b32 v[98:99], v63 offset0:30 offset1:31
	s_waitcnt lgkmcnt(4)
	v_cvt_pk_bf16_f32 v59, v88, v90
	global_store_dwordx4 v[64:65], v[56:59], off nt
	s_and_b64 vcc, exec, s[8:9]
	s_mov_b64 s[14:15], s[6:7]
	v_add_u32_e32 v56, 64, v62
	v_ashrrev_i32_e32 v57, 31, v56
	v_lshlrev_b64 v[64:65], 9, v[56:57]
	v_cvt_pk_bf16_f32 v56, v67, v69
	v_lshl_add_u64 v[64:65], v[60:61], 0, v[64:65]
	v_cvt_pk_bf16_f32 v57, v71, v73
	v_cvt_pk_bf16_f32 v58, v85, v87
	v_cvt_pk_bf16_f32 v59, v89, v91
	global_store_dwordx4 v[64:65], v[56:59], off nt
	s_nop 1
	v_add_u32_e32 v56, 0x80, v62
	v_ashrrev_i32_e32 v57, 31, v56
	v_lshlrev_b64 v[64:65], 9, v[56:57]
	v_cvt_pk_bf16_f32 v56, v74, v78
	v_lshl_add_u64 v[64:65], v[60:61], 0, v[64:65]
	v_cvt_pk_bf16_f32 v57, v80, v82
	s_waitcnt lgkmcnt(2)
	v_cvt_pk_bf16_f32 v58, v92, v94
	s_waitcnt lgkmcnt(0)
	v_cvt_pk_bf16_f32 v59, v96, v98
	global_store_dwordx4 v[64:65], v[56:59], off nt
	s_nop 1
	v_add_u32_e32 v56, 0xc0, v62
	v_ashrrev_i32_e32 v57, 31, v56
	v_lshlrev_b64 v[62:63], 9, v[56:57]
	v_lshl_add_u64 v[60:61], v[60:61], 0, v[62:63]
	v_cvt_pk_bf16_f32 v56, v75, v79
	v_cvt_pk_bf16_f32 v57, v81, v83
	v_cvt_pk_bf16_f32 v58, v93, v95
	v_cvt_pk_bf16_f32 v59, v97, v99
	global_store_dwordx4 v[60:61], v[56:59], off nt
	s_barrier
	s_cbranch_vccnz .LBB0_206
